# MoE: experts permuted per launch by row count (sorted snake) so every workgroup group gets 2 heavy + 2 light experts; P15 activations via LDS-DMA
# speedup vs baseline: 1.0275x; 1.0275x over previous
.LBB0_1312:
	s_cmp_lt_i32 s68, 16
	s_cselect_b64 s[0:1], -1, 0
	s_cmp_gt_i32 s69, 15
	s_cselect_b64 s[2:3], -1, 0
	s_and_b64 s[0:1], s[0:1], s[2:3]
	s_andn2_b64 vcc, exec, s[0:1]
	s_mov_b64 s[70:71], s[62:63]
	s_cbranch_vccnz .LBB0_1415
	s_waitcnt vmcnt(0) lgkmcnt(0)
	v_mov_b32_e32 v3, v0
	v_and_b32_e32 v20, 63, v3
	v_lshlrev_b32_e32 v21, 2, v20
	global_load_dword v22, v21, s[94:95] sc1
	s_waitcnt vmcnt(0)
	v_lshlrev_b32_e32 v22, 6, v22
	v_sub_u32_e32 v23, 63, v20
	v_or_b32_e32 v22, v22, v23
	v_mov_b32_e32 v24, 0
	v_readlane_b32 s0, v22, 0
	s_nop 1
	v_cmp_gt_u32_e32 vcc, s0, v22
	s_nop 1
	v_addc_co_u32_e32 v24, vcc, 0, v24, vcc
	v_readlane_b32 s0, v22, 1
	s_nop 1
	v_cmp_gt_u32_e32 vcc, s0, v22
	s_nop 1
	v_addc_co_u32_e32 v24, vcc, 0, v24, vcc
	v_readlane_b32 s0, v22, 2
	s_nop 1
	v_cmp_gt_u32_e32 vcc, s0, v22
	s_nop 1
	v_addc_co_u32_e32 v24, vcc, 0, v24, vcc
	v_readlane_b32 s0, v22, 3
	s_nop 1
	v_cmp_gt_u32_e32 vcc, s0, v22
	s_nop 1
	v_addc_co_u32_e32 v24, vcc, 0, v24, vcc
	v_readlane_b32 s0, v22, 4
	s_nop 1
	v_cmp_gt_u32_e32 vcc, s0, v22
	s_nop 1
	v_addc_co_u32_e32 v24, vcc, 0, v24, vcc
	v_readlane_b32 s0, v22, 5
	s_nop 1
	v_cmp_gt_u32_e32 vcc, s0, v22
	s_nop 1
	v_addc_co_u32_e32 v24, vcc, 0, v24, vcc
	v_readlane_b32 s0, v22, 6
	s_nop 1
	v_cmp_gt_u32_e32 vcc, s0, v22
	s_nop 1
	v_addc_co_u32_e32 v24, vcc, 0, v24, vcc
	v_readlane_b32 s0, v22, 7
	s_nop 1
	v_cmp_gt_u32_e32 vcc, s0, v22
	s_nop 1
	v_addc_co_u32_e32 v24, vcc, 0, v24, vcc
	v_readlane_b32 s0, v22, 8
	s_nop 1
	v_cmp_gt_u32_e32 vcc, s0, v22
	s_nop 1
	v_addc_co_u32_e32 v24, vcc, 0, v24, vcc
	v_readlane_b32 s0, v22, 9
	s_nop 1
	v_cmp_gt_u32_e32 vcc, s0, v22
	s_nop 1
	v_addc_co_u32_e32 v24, vcc, 0, v24, vcc
	v_readlane_b32 s0, v22, 10
	s_nop 1
	v_cmp_gt_u32_e32 vcc, s0, v22
	s_nop 1
	v_addc_co_u32_e32 v24, vcc, 0, v24, vcc
	v_readlane_b32 s0, v22, 11
	s_nop 1
	v_cmp_gt_u32_e32 vcc, s0, v22
	s_nop 1
	v_addc_co_u32_e32 v24, vcc, 0, v24, vcc
	v_readlane_b32 s0, v22, 12
	s_nop 1
	v_cmp_gt_u32_e32 vcc, s0, v22
	s_nop 1
	v_addc_co_u32_e32 v24, vcc, 0, v24, vcc
	v_readlane_b32 s0, v22, 13
	s_nop 1
	v_cmp_gt_u32_e32 vcc, s0, v22
	s_nop 1
	v_addc_co_u32_e32 v24, vcc, 0, v24, vcc
	v_readlane_b32 s0, v22, 14
	s_nop 1
	v_cmp_gt_u32_e32 vcc, s0, v22
	s_nop 1
	v_addc_co_u32_e32 v24, vcc, 0, v24, vcc
	v_readlane_b32 s0, v22, 15
	s_nop 1
	v_cmp_gt_u32_e32 vcc, s0, v22
	s_nop 1
	v_addc_co_u32_e32 v24, vcc, 0, v24, vcc
	v_readlane_b32 s0, v22, 16
	s_nop 1
	v_cmp_gt_u32_e32 vcc, s0, v22
	s_nop 1
	v_addc_co_u32_e32 v24, vcc, 0, v24, vcc
	v_readlane_b32 s0, v22, 17
	s_nop 1
	v_cmp_gt_u32_e32 vcc, s0, v22
	s_nop 1
	v_addc_co_u32_e32 v24, vcc, 0, v24, vcc
	v_readlane_b32 s0, v22, 18
	s_nop 1
	v_cmp_gt_u32_e32 vcc, s0, v22
	s_nop 1
	v_addc_co_u32_e32 v24, vcc, 0, v24, vcc
	v_readlane_b32 s0, v22, 19
	s_nop 1
	v_cmp_gt_u32_e32 vcc, s0, v22
	s_nop 1
	v_addc_co_u32_e32 v24, vcc, 0, v24, vcc
	v_readlane_b32 s0, v22, 20
	s_nop 1
	v_cmp_gt_u32_e32 vcc, s0, v22
	s_nop 1
	v_addc_co_u32_e32 v24, vcc, 0, v24, vcc
	v_readlane_b32 s0, v22, 21
	s_nop 1
	v_cmp_gt_u32_e32 vcc, s0, v22
	s_nop 1
	v_addc_co_u32_e32 v24, vcc, 0, v24, vcc
	v_readlane_b32 s0, v22, 22
	s_nop 1
	v_cmp_gt_u32_e32 vcc, s0, v22
	s_nop 1
	v_addc_co_u32_e32 v24, vcc, 0, v24, vcc
	v_readlane_b32 s0, v22, 23
	s_nop 1
	v_cmp_gt_u32_e32 vcc, s0, v22
	s_nop 1
	v_addc_co_u32_e32 v24, vcc, 0, v24, vcc
	v_readlane_b32 s0, v22, 24
	s_nop 1
	v_cmp_gt_u32_e32 vcc, s0, v22
	s_nop 1
	v_addc_co_u32_e32 v24, vcc, 0, v24, vcc
	v_readlane_b32 s0, v22, 25
	s_nop 1
	v_cmp_gt_u32_e32 vcc, s0, v22
	s_nop 1
	v_addc_co_u32_e32 v24, vcc, 0, v24, vcc
	v_readlane_b32 s0, v22, 26
	s_nop 1
	v_cmp_gt_u32_e32 vcc, s0, v22
	s_nop 1
	v_addc_co_u32_e32 v24, vcc, 0, v24, vcc
	v_readlane_b32 s0, v22, 27
	s_nop 1
	v_cmp_gt_u32_e32 vcc, s0, v22
	s_nop 1
	v_addc_co_u32_e32 v24, vcc, 0, v24, vcc
	v_readlane_b32 s0, v22, 28
	s_nop 1
	v_cmp_gt_u32_e32 vcc, s0, v22
	s_nop 1
	v_addc_co_u32_e32 v24, vcc, 0, v24, vcc
	v_readlane_b32 s0, v22, 29
	s_nop 1
	v_cmp_gt_u32_e32 vcc, s0, v22
	s_nop 1
	v_addc_co_u32_e32 v24, vcc, 0, v24, vcc
	v_readlane_b32 s0, v22, 30
	s_nop 1
	v_cmp_gt_u32_e32 vcc, s0, v22
	s_nop 1
	v_addc_co_u32_e32 v24, vcc, 0, v24, vcc
	v_readlane_b32 s0, v22, 31
	s_nop 1
	v_cmp_gt_u32_e32 vcc, s0, v22
	s_nop 1
	v_addc_co_u32_e32 v24, vcc, 0, v24, vcc
	v_readlane_b32 s0, v22, 32
	s_nop 1
	v_cmp_gt_u32_e32 vcc, s0, v22
	s_nop 1
	v_addc_co_u32_e32 v24, vcc, 0, v24, vcc
	v_readlane_b32 s0, v22, 33
	s_nop 1
	v_cmp_gt_u32_e32 vcc, s0, v22
	s_nop 1
	v_addc_co_u32_e32 v24, vcc, 0, v24, vcc
	v_readlane_b32 s0, v22, 34
	s_nop 1
	v_cmp_gt_u32_e32 vcc, s0, v22
	s_nop 1
	v_addc_co_u32_e32 v24, vcc, 0, v24, vcc
	v_readlane_b32 s0, v22, 35
	s_nop 1
	v_cmp_gt_u32_e32 vcc, s0, v22
	s_nop 1
	v_addc_co_u32_e32 v24, vcc, 0, v24, vcc
	v_readlane_b32 s0, v22, 36
	s_nop 1
	v_cmp_gt_u32_e32 vcc, s0, v22
	s_nop 1
	v_addc_co_u32_e32 v24, vcc, 0, v24, vcc
	v_readlane_b32 s0, v22, 37
	s_nop 1
	v_cmp_gt_u32_e32 vcc, s0, v22
	s_nop 1
	v_addc_co_u32_e32 v24, vcc, 0, v24, vcc
	v_readlane_b32 s0, v22, 38
	s_nop 1
	v_cmp_gt_u32_e32 vcc, s0, v22
	s_nop 1
	v_addc_co_u32_e32 v24, vcc, 0, v24, vcc
	v_readlane_b32 s0, v22, 39
	s_nop 1
	v_cmp_gt_u32_e32 vcc, s0, v22
	s_nop 1
	v_addc_co_u32_e32 v24, vcc, 0, v24, vcc
	v_readlane_b32 s0, v22, 40
	s_nop 1
	v_cmp_gt_u32_e32 vcc, s0, v22
	s_nop 1
	v_addc_co_u32_e32 v24, vcc, 0, v24, vcc
	v_readlane_b32 s0, v22, 41
	s_nop 1
	v_cmp_gt_u32_e32 vcc, s0, v22
	s_nop 1
	v_addc_co_u32_e32 v24, vcc, 0, v24, vcc
	v_readlane_b32 s0, v22, 42
	s_nop 1
	v_cmp_gt_u32_e32 vcc, s0, v22
	s_nop 1
	v_addc_co_u32_e32 v24, vcc, 0, v24, vcc
	v_readlane_b32 s0, v22, 43
	s_nop 1
	v_cmp_gt_u32_e32 vcc, s0, v22
	s_nop 1
	v_addc_co_u32_e32 v24, vcc, 0, v24, vcc
	v_readlane_b32 s0, v22, 44
	s_nop 1
	v_cmp_gt_u32_e32 vcc, s0, v22
	s_nop 1
	v_addc_co_u32_e32 v24, vcc, 0, v24, vcc
	v_readlane_b32 s0, v22, 45
	s_nop 1
	v_cmp_gt_u32_e32 vcc, s0, v22
	s_nop 1
	v_addc_co_u32_e32 v24, vcc, 0, v24, vcc
	v_readlane_b32 s0, v22, 46
	s_nop 1
	v_cmp_gt_u32_e32 vcc, s0, v22
	s_nop 1
	v_addc_co_u32_e32 v24, vcc, 0, v24, vcc
	v_readlane_b32 s0, v22, 47
	s_nop 1
	v_cmp_gt_u32_e32 vcc, s0, v22
	s_nop 1
	v_addc_co_u32_e32 v24, vcc, 0, v24, vcc
	v_readlane_b32 s0, v22, 48
	s_nop 1
	v_cmp_gt_u32_e32 vcc, s0, v22
	s_nop 1
	v_addc_co_u32_e32 v24, vcc, 0, v24, vcc
	v_readlane_b32 s0, v22, 49
	s_nop 1
	v_cmp_gt_u32_e32 vcc, s0, v22
	s_nop 1
	v_addc_co_u32_e32 v24, vcc, 0, v24, vcc
	v_readlane_b32 s0, v22, 50
	s_nop 1
	v_cmp_gt_u32_e32 vcc, s0, v22
	s_nop 1
	v_addc_co_u32_e32 v24, vcc, 0, v24, vcc
	v_readlane_b32 s0, v22, 51
	s_nop 1
	v_cmp_gt_u32_e32 vcc, s0, v22
	s_nop 1
	v_addc_co_u32_e32 v24, vcc, 0, v24, vcc
	v_readlane_b32 s0, v22, 52
	s_nop 1
	v_cmp_gt_u32_e32 vcc, s0, v22
	s_nop 1
	v_addc_co_u32_e32 v24, vcc, 0, v24, vcc
	v_readlane_b32 s0, v22, 53
	s_nop 1
	v_cmp_gt_u32_e32 vcc, s0, v22
	s_nop 1
	v_addc_co_u32_e32 v24, vcc, 0, v24, vcc
	v_readlane_b32 s0, v22, 54
	s_nop 1
	v_cmp_gt_u32_e32 vcc, s0, v22
	s_nop 1
	v_addc_co_u32_e32 v24, vcc, 0, v24, vcc
	v_readlane_b32 s0, v22, 55
	s_nop 1
	v_cmp_gt_u32_e32 vcc, s0, v22
	s_nop 1
	v_addc_co_u32_e32 v24, vcc, 0, v24, vcc
	v_readlane_b32 s0, v22, 56
	s_nop 1
	v_cmp_gt_u32_e32 vcc, s0, v22
	s_nop 1
	v_addc_co_u32_e32 v24, vcc, 0, v24, vcc
	v_readlane_b32 s0, v22, 57
	s_nop 1
	v_cmp_gt_u32_e32 vcc, s0, v22
	s_nop 1
	v_addc_co_u32_e32 v24, vcc, 0, v24, vcc
	v_readlane_b32 s0, v22, 58
	s_nop 1
	v_cmp_gt_u32_e32 vcc, s0, v22
	s_nop 1
	v_addc_co_u32_e32 v24, vcc, 0, v24, vcc
	v_readlane_b32 s0, v22, 59
	s_nop 1
	v_cmp_gt_u32_e32 vcc, s0, v22
	s_nop 1
	v_addc_co_u32_e32 v24, vcc, 0, v24, vcc
	v_readlane_b32 s0, v22, 60
	s_nop 1
	v_cmp_gt_u32_e32 vcc, s0, v22
	s_nop 1
	v_addc_co_u32_e32 v24, vcc, 0, v24, vcc
	v_readlane_b32 s0, v22, 61
	s_nop 1
	v_cmp_gt_u32_e32 vcc, s0, v22
	s_nop 1
	v_addc_co_u32_e32 v24, vcc, 0, v24, vcc
	v_readlane_b32 s0, v22, 62
	s_nop 1
	v_cmp_gt_u32_e32 vcc, s0, v22
	s_nop 1
	v_addc_co_u32_e32 v24, vcc, 0, v24, vcc
	v_readlane_b32 s0, v22, 63
	s_nop 1
	v_cmp_gt_u32_e32 vcc, s0, v22
	s_nop 1
	v_addc_co_u32_e32 v24, vcc, 0, v24, vcc
	s_lshr_b32 s1, s65, 4
	v_cmp_eq_u32_e32 vcc, s1, v24
	s_nop 3
	s_ff1_i32_b64 s100, vcc
	s_sub_i32 s2, 31, s1
	v_cmp_eq_u32_e32 vcc, s2, v24
	s_nop 3
	s_ff1_i32_b64 s0, vcc
	s_lshl_b32 s0, s0, 8
	s_or_b32 s100, s100, s0
	s_add_i32 s2, s1, 32
	v_cmp_eq_u32_e32 vcc, s2, v24
	s_nop 3
	s_ff1_i32_b64 s0, vcc
	s_lshl_b32 s0, s0, 16
	s_or_b32 s100, s100, s0
	s_sub_i32 s2, 63, s1
	v_cmp_eq_u32_e32 vcc, s2, v24
	s_nop 3
	s_ff1_i32_b64 s0, vcc
	s_lshl_b32 s0, s0, 24
	s_or_b32 s100, s100, s0
	s_cmpk_gt_i32 s65, 0x3ff
	v_and_b32_e32 v2, 15, v3
	v_mul_lo_u32 v1, v2, s33
	v_add_u32_e32 v1, s65, v1
	v_lshrrev_b32_e32 v1, 2, v1
	v_and_b32_e32 v4, 0xfc, v1
	v_and_b32_e32 v20, 3, v2
	v_lshlrev_b32_e32 v20, 3, v20
	v_lshrrev_b32_e64 v4, v20, s100
	v_and_b32_e32 v4, 0xff, v4
	v_lshlrev_b32_e32 v4, 2, v4
	global_load_dword v1, v4, s[94:95] sc1
	global_load_dword v172, v4, s[94:95] offset:256 sc1
	s_cbranch_scc1 .LBB0_1361
	s_add_u32 s24, s94, 0x43000000
	s_addc_u32 s25, s95, 0
	s_add_u32 s0, s94, 0x4b000000
	v_readlane_b32 s2, v254, 0
	s_addc_u32 s1, s95, 0
	v_bfe_u32 v4, v3, 4, 2
	s_lshr_b32 s2, s2, 8
	v_lshlrev_b32_e32 v5, 4, v2
	v_lshlrev_b32_e32 v6, 4, v3
	s_lshl_b32 s3, s2, 1
	v_lshl_or_b32 v173, v4, 14, v5
	v_ashrrev_i32_e32 v5, 3, v3
	v_and_b32_e32 v6, 0x70, v6
	s_add_i32 s3, s3, s97
	v_lshl_or_b32 v174, v5, 12, v6
	v_lshlrev_b32_e32 v6, 7, v5
	v_xor_b32_e32 v5, v5, v3
	v_bfe_u32 v175, v3, 5, 1
	v_and_b32_e32 v10, 7, v3
	v_lshlrev_b32_e32 v11, 2, v3
	v_bitop3_b32 v3, v4, v3, 7 bitop3:0x78
	v_lshrrev_b32_e32 v13, 2, v2
	s_and_b32 s26, s3, 3
	v_xor_b32_e32 v13, v3, v13
	v_lshlrev_b32_e32 v12, 7, v2
	s_lshl_b32 s3, s26, 11
	s_lshl_b32 s4, s2, 12
	v_lshlrev_b32_e32 v13, 4, v13
	v_lshl_add_u32 v3, v3, 4, 0
	v_lshlrev_b32_e32 v5, 4, v5
	v_lshlrev_b32_e32 v8, 3, v4
	v_add3_u32 v176, v3, v12, s3
	v_or3_b32 v3, v13, s4, v12
	v_and_b32_e32 v5, 0x70, v5
	v_lshlrev_b32_e32 v7, 9, v2
	v_bitop3_b32 v4, v4, v10, 4 bitop3:0x36
	s_add_i32 s5, s4, 0xc000
	v_add_u32_e32 v3, 0, v3
	v_lshl_or_b32 v201, v2, 11, v8
	v_mov_b32_e32 v2, 0
	v_and_b32_e32 v9, 8, v8
	v_or3_b32 v14, v13, s5, v12
	v_add_u32_e32 v178, 0xc000, v3
	v_add_u32_e32 v179, 0x1c000, v3
	v_lshl_add_u32 v3, v4, 4, 0
	v_add3_u32 v184, 0, v5, v6
	v_sub_u32_e32 v187, v184, v5
	v_lshl_or_b32 v187, v187, 5, v5
	s_mul_i32 s98, s97, 0x400
	s_mov_b32 s99, s98
	s_bitset1_b32 s99, 16
	v_mov_b32_e32 v4, v2
	v_mov_b32_e32 v5, v2
	v_add3_u32 v180, v3, v12, s3
	v_xad_u32 v182, v14, 64, 0
	v_add3_u32 v185, 0, v7, v9
	v_bitop3_b32 v192, v11, v10, 4 bitop3:0x6c
	v_mov_b32_e32 v3, v2
	v_mbcnt_lo_u32_b32 v6, -1, 0
	v_mov_b64_e32 v[18:19], v[4:5]
	v_mov_b64_e32 v[14:15], v[4:5]
	v_mov_b64_e32 v[10:11], v[4:5]
	s_mov_b32 s7, 0x20000
	s_or_b32 s30, s26, 4
	s_or_b32 s34, s26, 8
	s_or_b32 s36, s26, 12
	s_or_b32 s38, s26, 16
	v_mbcnt_hi_u32_b32 v193, -1, v6
	v_mov_b64_e32 v[16:17], v[2:3]
	v_mov_b64_e32 v[12:13], v[2:3]
	v_mov_b64_e32 v[8:9], v[2:3]
	v_mov_b64_e32 v[6:7], v[4:5]
	s_mov_b32 s27, 0
	v_add_u32_e32 v177, 0x10000, v176
	v_add_u32_e32 v181, 0x10000, v180
	v_add_u32_e32 v183, 0x10000, v182
	v_add_u32_e32 v186, 0x10000, v184
	s_and_b32 s1, s1, 0xffff
	s_brev_b32 s10, -2
	s_mov_b32 s11, s7
	s_lshl_b32 s28, s26, 14
	s_lshl_b32 s29, s2, 6
	s_lshl_b32 s31, s30, 14
	s_lshl_b32 s35, s34, 14
	s_lshl_b32 s37, s36, 14
	s_lshl_b32 s39, s38, 14
	s_mov_b64 s[16:17], 0
	s_mov_b32 s40, 0x40000
	s_mov_b32 s41, 0x80000
	s_mov_b32 s42, 0xc0000
	s_mov_b32 s43, 0x100000
	s_movk_i32 s44, 0x1000
	s_movk_i32 s45, 0x2000
	s_movk_i32 s46, 0x3000
	s_movk_i32 s47, 0x80
	s_mov_b32 s48, 0x40080
	s_mov_b32 s49, 0x80080
	s_mov_b32 s50, 0xc0080
	s_mov_b32 s51, 0x100080
	s_mov_b32 s52, 0x41000
	s_mov_b32 s53, 0x42000
	s_mov_b32 s54, 0x43000
	s_mov_b32 s6, s65
	v_mov_b64_e32 v[4:5], v[2:3]
	s_branch .LBB0_1316

.LBB0_1316:
	s_and_b32 s2, s27, 3
	s_lshl_b32 s2, s2, 3
	s_lshr_b32 s2, s100, s2
	s_and_b32 s2, s2, 0xff
	s_cmp_gt_u32 s27, 15
	s_cselect_b64 s[4:5], -1, 0
	s_mov_b64 s[8:9], -1
	s_and_b64 vcc, exec, s[4:5]
	s_cbranch_vccnz .LBB0_1357
	s_andn2_b64 vcc, exec, s[8:9]
	v_and_or_b32 v3, v193, 64, s27
	s_cbranch_vccz .LBB0_1358

.LBB0_1321:
	s_add_i32 s56, s6, s33
	s_cmpk_lt_i32 s56, 0x400
	s_cselect_b64 s[20:21], -1, 0
	s_cmpk_gt_i32 s56, 0x3ff
	s_cselect_b64 s[18:19], -1, 0
	s_cmp_lt_i32 s55, 1
	s_cbranch_scc1 .LBB0_1360
	v_readlane_b32 s72, v254, 5
	s_lshl_b32 s3, s6, 6
	v_readlane_b32 s84, v254, 17
	v_readlane_b32 s85, v254, 18
	s_and_b32 s58, s3, 0x3c0
	s_ashr_i32 s3, s2, 31
	s_and_b32 s4, s97, 1
	v_readlane_b32 s86, v254, 19
	v_readlane_b32 s87, v254, 20
	s_mov_b64 s[12:13], s[84:85]
	s_cmp_eq_u32 s4, 0
	s_mov_b64 s[14:15], s[86:87]
	s_cselect_b32 s5, s13, s15
	s_cselect_b32 s6, s12, s14
	s_lshl_b64 s[2:3], s[2:3], 23
	s_add_u32 s2, s6, s2
	s_addc_u32 s3, s5, s3
	s_lshl_b32 s8, s58, 2
	s_add_u32 s8, s2, s8
	s_addc_u32 s9, s3, 0
	s_lshl_b32 s2, s97, 3
	s_and_b32 s2, s2, -16
	s_ashr_i32 s3, s2, 31
	s_lshl_b64 s[2:3], s[2:3], 12
	s_add_u32 s8, s8, s2
	s_addc_u32 s9, s9, s3
	v_lshl_add_u32 v20, s4, 13, v185
	s_add_i32 s4, s27, 1
	s_and_b32 s4, s4, 3
	s_lshl_b32 s4, s4, 3
	s_lshr_b32 s4, s100, s4
	s_and_b32 s4, s4, 0xff
	s_lshl_b32 s4, s4, 23
	s_and_b32 s9, s9, 0xffff
	s_and_b32 s12, s97, 0xffffffe
	s_add_u32 s4, s6, s4
	s_addc_u32 s5, s5, 0
	s_lshl_b32 s6, s56, 8
	s_and_b32 s6, s6, 0xf00
	s_add_u32 s4, s4, s6
	v_bitop3_b32 v3, s12, v192, v175 bitop3:0x36
	s_addc_u32 s5, s5, 0
	v_lshlrev_b32_e32 v21, 4, v3
	s_add_u32 s12, s4, s2
	v_add_u32_e32 v3, v20, v21
	v_xad_u32 v194, v21, 16, v20
	v_xad_u32 v195, v21, 32, v20
	v_xad_u32 v196, v21, 48, v20
	s_addc_u32 s2, s5, s3
	s_mov_b32 s59, 0
	v_add_u32_e32 v197, 0x1c000, v3
	v_add_u32_e32 v198, 0x1c080, v194
	v_add_u32_e32 v199, 0x1c100, v195
	v_add_u32_e32 v200, 0x1c180, v196
	s_and_b32 s13, s2, 0xffff
	s_or_b32 s62, s58, 16
	v_readlane_b32 s73, v254, 6
	v_readlane_b32 s74, v254, 7
	v_readlane_b32 s75, v254, 8
	v_readlane_b32 s76, v254, 9
	v_readlane_b32 s77, v254, 10
	v_readlane_b32 s78, v254, 11
	v_readlane_b32 s79, v254, 12
	v_readlane_b32 s80, v254, 13
	v_readlane_b32 s81, v254, 14
	v_readlane_b32 s82, v254, 15
	v_readlane_b32 s83, v254, 16

.LBB0_1326:
	buffer_load_dwordx4 v[242:245], v173, s[8:11], s40 offen
	buffer_load_dwordx4 v[246:249], v173, s[8:11], s52 offen
	buffer_load_dwordx4 v[250:253], v173, s[8:11], s53 offen
	buffer_load_dwordx4 v[188:191], v173, s[8:11], s54 offen
	s_waitcnt vmcnt(4)
	ds_write_b128 v184, v[36:39]
	ds_write_b128 v184, v[40:43] offset:8192
	ds_write_b128 v184, v[44:47] offset:16384
	ds_write_b128 v184, v[48:51] offset:24576
	ds_write_b128 v184, v[52:55] offset:32768
	v_cvt_pk_bf16_f32 v36, v32, v28
	v_cvt_pk_bf16_f32 v37, v24, v20
	ds_write_b64 v3, v[36:37] offset:49152
	v_cvt_pk_bf16_f32 v20, v33, v29
	v_cvt_pk_bf16_f32 v21, v25, v21
	ds_write_b64 v194, v[20:21] offset:49280
	v_cvt_pk_bf16_f32 v20, v34, v30
	v_cvt_pk_bf16_f32 v21, v26, v22
	ds_write_b64 v195, v[20:21] offset:49408
	v_cvt_pk_bf16_f32 v20, v35, v31
	v_cvt_pk_bf16_f32 v21, v27, v23
	ds_write_b64 v196, v[20:21] offset:49536
	s_waitcnt lgkmcnt(0)
	s_barrier
	s_mov_b32 m0, s99
	s_nop 0
	buffer_load_dwordx4 v187, s[4:7], s47 offen lds
	s_add_i32 m0, s99, 0x2000
	s_nop 0
	buffer_load_dwordx4 v187, s[4:7], s48 offen lds
	s_add_i32 m0, s99, 0x4000
	s_nop 0
	buffer_load_dwordx4 v187, s[4:7], s49 offen lds
	s_add_i32 m0, s99, 0x6000
	s_nop 0
	buffer_load_dwordx4 v187, s[4:7], s50 offen lds
	s_add_i32 m0, s99, 0x8000
	s_nop 0
	buffer_load_dwordx4 v187, s[4:7], s51 offen lds
	ds_read_b128 v[92:95], v176 offset:0
	ds_read_b128 v[76:79], v176 offset:0x2000
	ds_read_b128 v[64:67], v176 offset:0x4000
	ds_read_b128 v[60:63], v176 offset:0x6000
	ds_read_b128 v[56:59], v176 offset:0x8000
	ds_read_b128 v[68:71], v178 offset:0
	ds_read_b128 v[72:75], v182 offset:0x800
	ds_read_b128 v[80:83], v178 offset:0x2000
	ds_read_b128 v[84:87], v182 offset:0x2800
	v_mov_b32_e32 v88, 0
	s_mov_b32 s2, -2
	s_mov_b32 s3, 0xc3000
	s_mov_b32 s14, 0x100180
	v_mov_b32_e32 v89, v88
	v_mov_b32_e32 v90, v88
	v_mov_b32_e32 v91, v88
	v_mov_b32_e32 v96, v88
	v_mov_b32_e32 v97, v88
	v_mov_b32_e32 v98, v88
	v_mov_b32_e32 v99, v88
	v_mov_b32_e32 v100, v88
	v_mov_b32_e32 v101, v88
	v_mov_b32_e32 v102, v88
	v_mov_b32_e32 v103, v88
	v_mov_b32_e32 v104, v88
	v_mov_b32_e32 v105, v88
	v_mov_b32_e32 v106, v88
	v_mov_b32_e32 v107, v88
	v_mov_b32_e32 v108, v88
	v_mov_b32_e32 v109, v88
	v_mov_b32_e32 v110, v88
	v_mov_b32_e32 v111, v88
	v_mov_b32_e32 v112, v88
	v_mov_b32_e32 v113, v88
	v_mov_b32_e32 v114, v88
	v_mov_b32_e32 v115, v88
	v_mov_b32_e32 v116, v88
	v_mov_b32_e32 v117, v88
	v_mov_b32_e32 v118, v88
	v_mov_b32_e32 v119, v88
	v_mov_b32_e32 v120, v88
	v_mov_b32_e32 v121, v88
	v_mov_b32_e32 v122, v88
	v_mov_b32_e32 v123, v88
	v_mov_b32_e32 v124, v88
	v_mov_b32_e32 v125, v88
	v_mov_b32_e32 v126, v88
	v_mov_b32_e32 v127, v88
	v_mov_b32_e32 v128, v88
	v_mov_b32_e32 v129, v88
	v_mov_b32_e32 v130, v88
	v_mov_b32_e32 v131, v88
	v_mov_b32_e32 v132, v88
	v_mov_b32_e32 v133, v88
	v_mov_b32_e32 v134, v88
	v_mov_b32_e32 v135, v88
	v_mov_b32_e32 v136, v88
	v_mov_b32_e32 v137, v88
	v_mov_b32_e32 v138, v88
	v_mov_b32_e32 v139, v88
	v_mov_b32_e32 v140, v88
	v_mov_b32_e32 v141, v88
	v_mov_b32_e32 v142, v88
	v_mov_b32_e32 v143, v88
	v_mov_b32_e32 v144, v88
	v_mov_b32_e32 v145, v88
	v_mov_b32_e32 v146, v88
	v_mov_b32_e32 v147, v88
	v_mov_b32_e32 v148, v88
	v_mov_b32_e32 v149, v88
	v_mov_b32_e32 v150, v88
	v_mov_b32_e32 v151, v88
	v_mov_b32_e32 v152, v88
	v_mov_b32_e32 v153, v88
	v_mov_b32_e32 v154, v88
	v_mov_b32_e32 v155, v88
	v_mov_b32_e32 v156, v88
	v_mov_b32_e32 v157, v88
	v_mov_b32_e32 v158, v88
	v_mov_b32_e32 v159, v88
	v_mov_b32_e32 v160, v88
	v_mov_b32_e32 v161, v88
	v_mov_b32_e32 v162, v88
	v_mov_b32_e32 v163, v88
	v_mov_b32_e32 v164, v88
	v_mov_b32_e32 v165, v88
	v_mov_b32_e32 v166, v88
	v_mov_b32_e32 v167, v88
	v_mov_b32_e32 v168, v88
	v_mov_b32_e32 v169, v88
	v_mov_b32_e32 v170, v88
	v_mov_b32_e32 v171, v88
.LBB0_1327:
	ds_read_b128 v[202:205], v180 offset:0
	ds_read_b128 v[206:209], v180 offset:0x2000
	ds_read_b128 v[210:213], v180 offset:0x4000
	ds_read_b128 v[214:217], v180 offset:0x6000
	ds_read_b128 v[218:221], v180 offset:0x8000
	ds_read_b128 v[222:225], v182 offset:0
	ds_read_b128 v[226:229], v178 offset:0x800
	ds_read_b128 v[230:233], v182 offset:0x2000
	ds_read_b128 v[234:237], v178 offset:0x2800
	s_waitcnt lgkmcnt(9)
	s_nop 1
	v_mfma_f32_16x16x32_bf16 v[168:171], v[68:71], v[92:95], v[168:171]
	v_mfma_f32_16x16x32_bf16 v[164:167], v[72:75], v[92:95], v[164:167]
	s_add_i32 s15, s3, 0xfffbd000
	buffer_load_dwordx4 v[24:27], v173, s[8:11], s15 offen
	v_mfma_f32_16x16x32_bf16 v[160:163], v[80:83], v[92:95], v[160:163]
	v_mfma_f32_16x16x32_bf16 v[92:95], v[84:87], v[92:95], v[156:159]
	v_mfma_f32_16x16x32_bf16 v[152:155], v[68:71], v[76:79], v[152:155]
	v_mfma_f32_16x16x32_bf16 v[148:151], v[72:75], v[76:79], v[148:151]
	v_mfma_f32_16x16x32_bf16 v[144:147], v[80:83], v[76:79], v[144:147]
	s_add_i32 s64, s3, 0xfffbe000
	buffer_load_dwordx4 v[32:35], v173, s[8:11], s64 offen
	v_mfma_f32_16x16x32_bf16 v[76:79], v[84:87], v[76:79], v[140:143]
	v_mfma_f32_16x16x32_bf16 v[136:139], v[68:71], v[64:67], v[136:139]
	v_mfma_f32_16x16x32_bf16 v[132:135], v[72:75], v[64:67], v[132:135]
	v_mfma_f32_16x16x32_bf16 v[128:131], v[80:83], v[64:67], v[128:131]
	v_mfma_f32_16x16x32_bf16 v[64:67], v[84:87], v[64:67], v[124:127]
	s_add_i32 s15, s3, 0xfffbf000
	buffer_load_dwordx4 v[20:23], v173, s[8:11], s15 offen
	v_mfma_f32_16x16x32_bf16 v[120:123], v[68:71], v[60:63], v[120:123]
	v_mfma_f32_16x16x32_bf16 v[116:119], v[72:75], v[60:63], v[116:119]
	v_mfma_f32_16x16x32_bf16 v[112:115], v[80:83], v[60:63], v[112:115]
	v_mfma_f32_16x16x32_bf16 v[60:63], v[84:87], v[60:63], v[108:111]
	v_mfma_f32_16x16x32_bf16 v[68:71], v[68:71], v[56:59], v[104:107]
	s_add_i32 s64, s3, 0xfffc0000
	buffer_load_dwordx4 v[28:31], v173, s[8:11], s64 offen
	v_mfma_f32_16x16x32_bf16 v[72:75], v[72:75], v[56:59], v[100:103]
	v_mfma_f32_16x16x32_bf16 v[80:83], v[80:83], v[56:59], v[96:99]
	v_mfma_f32_16x16x32_bf16 v[56:59], v[84:87], v[56:59], v[88:91]
	s_waitcnt vmcnt(4)
	v_cvt_pk_bf16_f32 v36, v242, v246
	v_cvt_pk_bf16_f32 v37, v250, v188
	ds_write_b64 v197, v[36:37]
	v_cvt_pk_bf16_f32 v36, v243, v247
	v_cvt_pk_bf16_f32 v37, v251, v189
	ds_write_b64 v198, v[36:37]
	v_cvt_pk_bf16_f32 v36, v244, v248
	v_cvt_pk_bf16_f32 v37, v252, v190
	ds_write_b64 v199, v[36:37]
	v_cvt_pk_bf16_f32 v36, v245, v249
	v_cvt_pk_bf16_f32 v37, v253, v191
	ds_write_b64 v200, v[36:37]
	s_waitcnt lgkmcnt(0)
	s_barrier
	s_nop 0
	v_mfma_f32_16x16x32_bf16 v[124:127], v[222:225], v[210:213], v[136:139]
	ds_read_b128 v[136:139], v177 offset:0
	ds_read_b128 v[140:143], v177 offset:0x2000
	v_mfma_f32_16x16x32_bf16 v[108:111], v[230:233], v[206:209], v[144:147]
	s_mov_b32 m0, s98
	s_add_i32 s15, s14, 0xffefff80
	buffer_load_dwordx4 v187, s[4:7], s15 offen lds
	ds_read_b128 v[144:147], v177 offset:0x4000
	v_mfma_f32_16x16x32_bf16 v[104:107], v[226:229], v[206:209], v[148:151]
	ds_read_b128 v[148:151], v177 offset:0x6000
	v_mfma_f32_16x16x32_bf16 v[100:103], v[222:225], v[206:209], v[152:155]
	ds_read_b128 v[152:155], v177 offset:0x8000
	ds_read_b128 v[156:159], v179 offset:0
	v_mfma_f32_16x16x32_bf16 v[96:99], v[230:233], v[202:205], v[160:163]
	ds_read_b128 v[160:163], v183 offset:0x800
	v_mfma_f32_16x16x32_bf16 v[84:87], v[222:225], v[202:205], v[168:171]
	s_add_i32 m0, s98, 0x2000
	s_add_i32 s64, s14, 0xfff3ff80
	buffer_load_dwordx4 v187, s[4:7], s64 offen lds
	v_mfma_f32_16x16x32_bf16 v[88:91], v[226:229], v[202:205], v[164:167]
	ds_read_b128 v[164:167], v179 offset:0x2000
	ds_read_b128 v[168:171], v183 offset:0x2800
	v_mfma_f32_16x16x32_bf16 v[92:95], v[234:237], v[202:205], v[92:95]
	v_mfma_f32_16x16x32_bf16 v[76:79], v[234:237], v[206:209], v[76:79]
	v_mfma_f32_16x16x32_bf16 v[132:135], v[226:229], v[210:213], v[132:135]
	s_add_i32 m0, s98, 0x4000
	s_add_i32 s15, s14, 0xfff7ff80
	buffer_load_dwordx4 v187, s[4:7], s15 offen lds
	v_mfma_f32_16x16x32_bf16 v[128:131], v[230:233], v[210:213], v[128:131]
	v_mfma_f32_16x16x32_bf16 v[64:67], v[234:237], v[210:213], v[64:67]
	v_mfma_f32_16x16x32_bf16 v[120:123], v[222:225], v[214:217], v[120:123]
	v_mfma_f32_16x16x32_bf16 v[116:119], v[226:229], v[214:217], v[116:119]
	s_add_i32 m0, s98, 0x6000
	s_add_i32 s64, s14, 0xfffbff80
	buffer_load_dwordx4 v187, s[4:7], s64 offen lds
	v_mfma_f32_16x16x32_bf16 v[112:115], v[230:233], v[214:217], v[112:115]
	v_mfma_f32_16x16x32_bf16 v[60:63], v[234:237], v[214:217], v[60:63]
	v_mfma_f32_16x16x32_bf16 v[68:71], v[222:225], v[218:221], v[68:71]
	v_mfma_f32_16x16x32_bf16 v[72:75], v[226:229], v[218:221], v[72:75]
	s_add_i32 m0, s98, 0x8000
	s_add_i32 s15, s14, 0xffffff80
	buffer_load_dwordx4 v187, s[4:7], s15 offen lds
	v_mfma_f32_16x16x32_bf16 v[80:83], v[230:233], v[218:221], v[80:83]
	v_mfma_f32_16x16x32_bf16 v[56:59], v[234:237], v[218:221], v[56:59]
	ds_read_b128 v[202:205], v181 offset:0
	ds_read_b128 v[206:209], v181 offset:0x2000
	ds_read_b128 v[210:213], v181 offset:0x4000
	ds_read_b128 v[214:217], v181 offset:0x6000
	ds_read_b128 v[218:221], v181 offset:0x8000
	ds_read_b128 v[222:225], v183 offset:0
	ds_read_b128 v[226:229], v179 offset:0x800
	ds_read_b128 v[230:233], v183 offset:0x2000
	ds_read_b128 v[234:237], v179 offset:0x2800
	s_waitcnt lgkmcnt(9)
	s_nop 0
	v_mfma_f32_16x16x32_bf16 v[84:87], v[156:159], v[136:139], v[84:87]
	v_mfma_f32_16x16x32_bf16 v[88:91], v[160:163], v[136:139], v[88:91]
	s_add_i32 s15, s3, 0xffffd000
	buffer_load_dwordx4 v[242:245], v173, s[8:11], s15 offen
	v_mfma_f32_16x16x32_bf16 v[96:99], v[164:167], v[136:139], v[96:99]
	v_mfma_f32_16x16x32_bf16 v[92:95], v[168:171], v[136:139], v[92:95]
	v_mfma_f32_16x16x32_bf16 v[100:103], v[156:159], v[140:143], v[100:103]
	v_mfma_f32_16x16x32_bf16 v[104:107], v[160:163], v[140:143], v[104:107]
	v_mfma_f32_16x16x32_bf16 v[108:111], v[164:167], v[140:143], v[108:111]
	s_add_i32 s64, s3, 0xffffe000
	buffer_load_dwordx4 v[246:249], v173, s[8:11], s64 offen
	v_mfma_f32_16x16x32_bf16 v[76:79], v[168:171], v[140:143], v[76:79]
	v_mfma_f32_16x16x32_bf16 v[124:127], v[156:159], v[144:147], v[124:127]
	v_mfma_f32_16x16x32_bf16 v[132:135], v[160:163], v[144:147], v[132:135]
	v_mfma_f32_16x16x32_bf16 v[128:131], v[164:167], v[144:147], v[128:131]
	v_mfma_f32_16x16x32_bf16 v[64:67], v[168:171], v[144:147], v[64:67]
	s_add_i32 s15, s3, 0xfffff000
	buffer_load_dwordx4 v[250:253], v173, s[8:11], s15 offen
	v_mfma_f32_16x16x32_bf16 v[120:123], v[156:159], v[148:151], v[120:123]
	v_mfma_f32_16x16x32_bf16 v[116:119], v[160:163], v[148:151], v[116:119]
	v_mfma_f32_16x16x32_bf16 v[112:115], v[164:167], v[148:151], v[112:115]
	v_mfma_f32_16x16x32_bf16 v[60:63], v[168:171], v[148:151], v[60:63]
	v_mfma_f32_16x16x32_bf16 v[68:71], v[156:159], v[152:155], v[68:71]
	buffer_load_dwordx4 v[188:191], v173, s[8:11], s3 offen
	v_mfma_f32_16x16x32_bf16 v[72:75], v[160:163], v[152:155], v[72:75]
	v_mfma_f32_16x16x32_bf16 v[80:83], v[164:167], v[152:155], v[80:83]
	v_mfma_f32_16x16x32_bf16 v[238:241], v[168:171], v[152:155], v[56:59]
	s_waitcnt vmcnt(4)
	v_cvt_pk_bf16_f32 v36, v24, v32
	v_cvt_pk_bf16_f32 v37, v20, v28
	ds_write_b64 v3, v[36:37] offset:49152
	v_cvt_pk_bf16_f32 v36, v25, v33
	v_cvt_pk_bf16_f32 v37, v21, v29
	ds_write_b64 v194, v[36:37] offset:49280
	v_cvt_pk_bf16_f32 v36, v26, v34
	v_cvt_pk_bf16_f32 v37, v22, v30
	ds_write_b64 v195, v[36:37] offset:49408
	v_cvt_pk_bf16_f32 v36, v27, v35
	v_cvt_pk_bf16_f32 v37, v23, v31
	ds_write_b64 v196, v[36:37] offset:49536
	s_waitcnt lgkmcnt(0)
	s_barrier
	s_nop 0
	v_mfma_f32_16x16x32_bf16 v[156:159], v[234:237], v[202:205], v[92:95]
	ds_read_b128 v[92:95], v176 offset:0
	v_mfma_f32_16x16x32_bf16 v[140:143], v[234:237], v[206:209], v[76:79]
	s_mov_b32 m0, s99
	s_add_i32 s15, s14, 0xfff00000
	buffer_load_dwordx4 v187, s[4:7], s15 offen lds
	ds_read_b128 v[76:79], v176 offset:0x2000
	v_mfma_f32_16x16x32_bf16 v[136:139], v[222:225], v[210:213], v[124:127]
	v_mfma_f32_16x16x32_bf16 v[124:127], v[234:237], v[210:213], v[64:67]
	ds_read_b128 v[64:67], v176 offset:0x4000
	v_mfma_f32_16x16x32_bf16 v[144:147], v[230:233], v[206:209], v[108:111]
	v_mfma_f32_16x16x32_bf16 v[108:111], v[234:237], v[214:217], v[60:63]
	s_add_i32 m0, s99, 0x2000
	s_add_i32 s64, s14, 0xfff40000
	buffer_load_dwordx4 v187, s[4:7], s64 offen lds
	ds_read_b128 v[60:63], v176 offset:0x6000
	ds_read_b128 v[56:59], v176 offset:0x8000
	v_mfma_f32_16x16x32_bf16 v[148:151], v[226:229], v[206:209], v[104:107]
	v_mfma_f32_16x16x32_bf16 v[104:107], v[222:225], v[218:221], v[68:71]
	ds_read_b128 v[68:71], v178 offset:0
	v_mfma_f32_16x16x32_bf16 v[152:155], v[222:225], v[206:209], v[100:103]
	v_mfma_f32_16x16x32_bf16 v[100:103], v[226:229], v[218:221], v[72:75]
	s_add_i32 m0, s99, 0x4000
	s_add_i32 s15, s14, 0xfff80000
	buffer_load_dwordx4 v187, s[4:7], s15 offen lds
	ds_read_b128 v[72:75], v182 offset:0x800
	v_mfma_f32_16x16x32_bf16 v[168:171], v[222:225], v[202:205], v[84:87]
	v_mfma_f32_16x16x32_bf16 v[164:167], v[226:229], v[202:205], v[88:91]
	v_mfma_f32_16x16x32_bf16 v[160:163], v[230:233], v[202:205], v[96:99]
	v_mfma_f32_16x16x32_bf16 v[132:135], v[226:229], v[210:213], v[132:135]
	s_add_i32 m0, s99, 0x6000
	s_add_i32 s64, s14, 0xfffc0000
	buffer_load_dwordx4 v187, s[4:7], s64 offen lds
	v_mfma_f32_16x16x32_bf16 v[128:131], v[230:233], v[210:213], v[128:131]
	v_mfma_f32_16x16x32_bf16 v[120:123], v[222:225], v[214:217], v[120:123]
	v_mfma_f32_16x16x32_bf16 v[116:119], v[226:229], v[214:217], v[116:119]
	v_mfma_f32_16x16x32_bf16 v[112:115], v[230:233], v[214:217], v[112:115]
	s_add_i32 m0, s99, 0x8000
	s_nop 0
	buffer_load_dwordx4 v187, s[4:7], s14 offen lds
	v_mfma_f32_16x16x32_bf16 v[96:99], v[230:233], v[218:221], v[80:83]
	ds_read_b128 v[80:83], v178 offset:0x2000
	ds_read_b128 v[84:87], v182 offset:0x2800
	v_mfma_f32_16x16x32_bf16 v[88:91], v[234:237], v[218:221], v[238:241]
	s_add_i32 s2, s2, 2
	s_add_i32 s3, s3, 0x80000
	s_addk_i32 s14, 0x100
	s_cmp_lt_u32 s2, 27
	s_cbranch_scc1 .LBB0_1327
	ds_read_b128 v[202:205], v180 offset:0
	ds_read_b128 v[206:209], v180 offset:0x2000
	ds_read_b128 v[210:213], v180 offset:0x4000
	ds_read_b128 v[214:217], v180 offset:0x6000
	ds_read_b128 v[218:221], v180 offset:0x8000
	ds_read_b128 v[222:225], v182 offset:0
	ds_read_b128 v[226:229], v178 offset:0x800
	ds_read_b128 v[230:233], v182 offset:0x2000
	ds_read_b128 v[234:237], v178 offset:0x2800
	s_waitcnt lgkmcnt(9)
	s_nop 0
	v_mfma_f32_16x16x32_bf16 v[168:171], v[68:71], v[92:95], v[168:171]
	v_mfma_f32_16x16x32_bf16 v[164:167], v[72:75], v[92:95], v[164:167]
	v_mfma_f32_16x16x32_bf16 v[160:163], v[80:83], v[92:95], v[160:163]
	v_mfma_f32_16x16x32_bf16 v[92:95], v[84:87], v[92:95], v[156:159]
	v_mfma_f32_16x16x32_bf16 v[152:155], v[68:71], v[76:79], v[152:155]
	v_mfma_f32_16x16x32_bf16 v[148:151], v[72:75], v[76:79], v[148:151]
	v_mfma_f32_16x16x32_bf16 v[144:147], v[80:83], v[76:79], v[144:147]
	v_mfma_f32_16x16x32_bf16 v[76:79], v[84:87], v[76:79], v[140:143]
	v_mfma_f32_16x16x32_bf16 v[136:139], v[68:71], v[64:67], v[136:139]
	v_mfma_f32_16x16x32_bf16 v[132:135], v[72:75], v[64:67], v[132:135]
	v_mfma_f32_16x16x32_bf16 v[128:131], v[80:83], v[64:67], v[128:131]
	v_mfma_f32_16x16x32_bf16 v[124:127], v[84:87], v[64:67], v[124:127]
	v_mfma_f32_16x16x32_bf16 v[120:123], v[68:71], v[60:63], v[120:123]
	v_mfma_f32_16x16x32_bf16 v[116:119], v[72:75], v[60:63], v[116:119]
	v_mfma_f32_16x16x32_bf16 v[112:115], v[80:83], v[60:63], v[112:115]
	v_mfma_f32_16x16x32_bf16 v[108:111], v[84:87], v[60:63], v[108:111]
	v_mfma_f32_16x16x32_bf16 v[104:107], v[68:71], v[56:59], v[104:107]
	v_mfma_f32_16x16x32_bf16 v[140:143], v[72:75], v[56:59], v[100:103]
	v_mfma_f32_16x16x32_bf16 v[156:159], v[80:83], v[56:59], v[96:99]
	v_mfma_f32_16x16x32_bf16 v[238:241], v[84:87], v[56:59], v[88:91]
	s_waitcnt vmcnt(0)
	v_cvt_pk_bf16_f32 v36, v242, v246
	v_cvt_pk_bf16_f32 v37, v250, v188
	ds_write_b64 v197, v[36:37]
	v_cvt_pk_bf16_f32 v36, v243, v247
	v_cvt_pk_bf16_f32 v37, v251, v189
	ds_write_b64 v198, v[36:37]
	v_cvt_pk_bf16_f32 v36, v244, v248
	v_cvt_pk_bf16_f32 v37, v252, v190
	ds_write_b64 v199, v[36:37]
	v_cvt_pk_bf16_f32 v36, v245, v249
	v_cvt_pk_bf16_f32 v37, v253, v191
	ds_write_b64 v200, v[36:37]
	s_waitcnt lgkmcnt(0)
	s_barrier
	s_nop 0
	v_mfma_f32_16x16x32_bf16 v[56:59], v[226:229], v[206:209], v[148:151]
	ds_read_b128 v[148:151], v177 offset:0
	v_mfma_f32_16x16x32_bf16 v[60:63], v[230:233], v[206:209], v[144:147]
	ds_read_b128 v[144:147], v177 offset:0x2000
	v_mfma_f32_16x16x32_bf16 v[80:83], v[234:237], v[210:213], v[124:127]
	ds_read_b128 v[124:127], v177 offset:0x4000
	v_mfma_f32_16x16x32_bf16 v[88:91], v[226:229], v[214:217], v[116:119]
	ds_read_b128 v[116:119], v177 offset:0x6000
	v_mfma_f32_16x16x32_bf16 v[96:99], v[234:237], v[214:217], v[108:111]
	ds_read_b128 v[108:111], v177 offset:0x8000
	v_mfma_f32_16x16x32_bf16 v[84:87], v[222:225], v[214:217], v[120:123]
	ds_read_b128 v[120:123], v179 offset:0
	v_mfma_f32_16x16x32_bf16 v[64:67], v[234:237], v[206:209], v[76:79]
	v_mfma_f32_16x16x32_bf16 v[76:79], v[230:233], v[210:213], v[128:131]
	ds_read_b128 v[128:131], v183 offset:0x800
	v_mfma_f32_16x16x32_bf16 v[20:23], v[222:225], v[202:205], v[168:171]
	v_mfma_f32_16x16x32_bf16 v[24:27], v[226:229], v[202:205], v[164:167]
	v_mfma_f32_16x16x32_bf16 v[28:31], v[230:233], v[202:205], v[160:163]
	v_mfma_f32_16x16x32_bf16 v[32:35], v[234:237], v[202:205], v[92:95]
	v_mfma_f32_16x16x32_bf16 v[52:55], v[222:225], v[206:209], v[152:155]
	v_mfma_f32_16x16x32_bf16 v[68:71], v[222:225], v[210:213], v[136:139]
	v_mfma_f32_16x16x32_bf16 v[72:75], v[226:229], v[210:213], v[132:135]
	ds_read_b128 v[132:135], v179 offset:0x2000
	ds_read_b128 v[136:139], v183 offset:0x2800
	v_mfma_f32_16x16x32_bf16 v[92:95], v[230:233], v[214:217], v[112:115]
	v_mfma_f32_16x16x32_bf16 v[100:103], v[222:225], v[218:221], v[104:107]
	v_mfma_f32_16x16x32_bf16 v[104:107], v[226:229], v[218:221], v[140:143]
	v_mfma_f32_16x16x32_bf16 v[112:115], v[230:233], v[218:221], v[156:159]
	v_mfma_f32_16x16x32_bf16 v[140:143], v[234:237], v[218:221], v[238:241]
	s_add_i32 s2, s59, 0x140
	s_cmp_ge_i32 s2, s55
	s_cselect_b64 s[2:3], -1, 0
	s_and_b64 s[2:3], s[20:21], s[2:3]
	v_mov_b64_e32 v[50:51], v[6:7]
	v_mov_b64_e32 v[46:47], v[10:11]
	v_mov_b64_e32 v[42:43], v[14:15]
	v_mov_b64_e32 v[38:39], v[18:19]
	s_andn2_b64 vcc, exec, s[2:3]
	v_mov_b64_e32 v[48:49], v[4:5]
	v_mov_b64_e32 v[44:45], v[8:9]
	v_mov_b64_e32 v[40:41], v[12:13]
	v_mov_b64_e32 v[36:37], v[16:17]
	s_cbranch_vccnz .LBB0_1330
	s_mov_b32 s14, s10
	s_mov_b32 s15, s11
	buffer_load_dwordx4 v[48:51], v173, s[12:15], 0 offen
	buffer_load_dwordx4 v[44:47], v173, s[12:15], s44 offen
	buffer_load_dwordx4 v[40:43], v173, s[12:15], s45 offen
	buffer_load_dwordx4 v[36:39], v173, s[12:15], s46 offen

.LBB0_1339:
	buffer_load_dwordx4 v[242:245], v173, s[8:11], s40 offen
	buffer_load_dwordx4 v[246:249], v173, s[8:11], s52 offen
	buffer_load_dwordx4 v[250:253], v173, s[8:11], s53 offen
	buffer_load_dwordx4 v[188:191], v173, s[8:11], s54 offen
	s_waitcnt vmcnt(4)
	ds_write_b128 v184, v[36:39]
	ds_write_b128 v184, v[40:43] offset:8192
	ds_write_b128 v184, v[44:47] offset:16384
	ds_write_b128 v184, v[48:51] offset:24576
	v_cvt_pk_bf16_f32 v36, v32, v28
	v_cvt_pk_bf16_f32 v37, v24, v20
	ds_write_b64 v3, v[36:37] offset:49152
	v_cvt_pk_bf16_f32 v20, v33, v29
	v_cvt_pk_bf16_f32 v21, v25, v21
	ds_write_b64 v194, v[20:21] offset:49280
	v_cvt_pk_bf16_f32 v20, v34, v30
	v_cvt_pk_bf16_f32 v21, v26, v22
	ds_write_b64 v195, v[20:21] offset:49408
	v_cvt_pk_bf16_f32 v52, v35, v31
	v_cvt_pk_bf16_f32 v53, v27, v23
	ds_write_b64 v196, v[52:53] offset:49536
	s_waitcnt lgkmcnt(0)
	s_barrier
	s_mov_b32 m0, s99
	s_nop 0
	buffer_load_dwordx4 v187, s[4:7], s47 offen lds
	s_add_i32 m0, s99, 0x2000
	s_nop 0
	buffer_load_dwordx4 v187, s[4:7], s48 offen lds
	s_add_i32 m0, s99, 0x4000
	s_nop 0
	buffer_load_dwordx4 v187, s[4:7], s49 offen lds
	s_add_i32 m0, s99, 0x6000
	s_nop 0
	buffer_load_dwordx4 v187, s[4:7], s50 offen lds
	ds_read_b128 v[72:75], v176 offset:0
	ds_read_b128 v[60:63], v176 offset:0x2000
	ds_read_b128 v[56:59], v176 offset:0x4000
	ds_read_b128 v[52:55], v176 offset:0x6000
	ds_read_b128 v[64:67], v178 offset:0
	ds_read_b128 v[68:71], v182 offset:0x800
	ds_read_b128 v[76:79], v178 offset:0x2000
	ds_read_b128 v[80:83], v182 offset:0x2800
	v_mov_b32_e32 v84, 0
	s_mov_b32 s2, -2
	s_mov_b32 s3, 0xc3000
	s_mov_b32 s14, 0xc0180
	v_mov_b32_e32 v85, v84
	v_mov_b32_e32 v86, v84
	v_mov_b32_e32 v87, v84
	v_mov_b32_e32 v88, v84
	v_mov_b32_e32 v89, v84
	v_mov_b32_e32 v90, v84
	v_mov_b32_e32 v91, v84
	v_mov_b32_e32 v92, v84
	v_mov_b32_e32 v93, v84
	v_mov_b32_e32 v94, v84
	v_mov_b32_e32 v95, v84
	v_mov_b32_e32 v96, v84
	v_mov_b32_e32 v97, v84
	v_mov_b32_e32 v98, v84
	v_mov_b32_e32 v99, v84
	v_mov_b32_e32 v100, v84
	v_mov_b32_e32 v101, v84
	v_mov_b32_e32 v102, v84
	v_mov_b32_e32 v103, v84
	v_mov_b32_e32 v104, v84
	v_mov_b32_e32 v105, v84
	v_mov_b32_e32 v106, v84
	v_mov_b32_e32 v107, v84
	v_mov_b32_e32 v108, v84
	v_mov_b32_e32 v109, v84
	v_mov_b32_e32 v110, v84
	v_mov_b32_e32 v111, v84
	v_mov_b32_e32 v112, v84
	v_mov_b32_e32 v113, v84
	v_mov_b32_e32 v114, v84
	v_mov_b32_e32 v115, v84
	v_mov_b32_e32 v116, v84
	v_mov_b32_e32 v117, v84
	v_mov_b32_e32 v118, v84
	v_mov_b32_e32 v119, v84
	v_mov_b32_e32 v120, v84
	v_mov_b32_e32 v121, v84
	v_mov_b32_e32 v122, v84
	v_mov_b32_e32 v123, v84
	v_mov_b32_e32 v124, v84
	v_mov_b32_e32 v125, v84
	v_mov_b32_e32 v126, v84
	v_mov_b32_e32 v127, v84
	v_mov_b32_e32 v128, v84
	v_mov_b32_e32 v129, v84
	v_mov_b32_e32 v130, v84
	v_mov_b32_e32 v131, v84
	v_mov_b32_e32 v132, v84
	v_mov_b32_e32 v133, v84
	v_mov_b32_e32 v134, v84
	v_mov_b32_e32 v135, v84
	v_mov_b32_e32 v136, v84
	v_mov_b32_e32 v137, v84
	v_mov_b32_e32 v138, v84
	v_mov_b32_e32 v139, v84
	v_mov_b32_e32 v140, v84
	v_mov_b32_e32 v141, v84
	v_mov_b32_e32 v142, v84
	v_mov_b32_e32 v143, v84
	v_mov_b32_e32 v144, v84
	v_mov_b32_e32 v145, v84
	v_mov_b32_e32 v146, v84
	v_mov_b32_e32 v147, v84
.LBB0_1340:
	ds_read_b128 v[148:151], v180 offset:0
	ds_read_b128 v[152:155], v180 offset:0x2000
	ds_read_b128 v[156:159], v180 offset:0x4000
	ds_read_b128 v[160:163], v180 offset:0x6000
	ds_read_b128 v[164:167], v182 offset:0
	ds_read_b128 v[168:171], v178 offset:0x800
	ds_read_b128 v[202:205], v182 offset:0x2000
	ds_read_b128 v[206:209], v178 offset:0x2800
	s_waitcnt lgkmcnt(8)
	s_nop 1
	v_mfma_f32_16x16x32_bf16 v[144:147], v[64:67], v[72:75], v[144:147]
	v_mfma_f32_16x16x32_bf16 v[140:143], v[68:71], v[72:75], v[140:143]
	s_add_i32 s15, s3, 0xfffbd000
	buffer_load_dwordx4 v[24:27], v173, s[8:11], s15 offen
	v_mfma_f32_16x16x32_bf16 v[136:139], v[76:79], v[72:75], v[136:139]
	v_mfma_f32_16x16x32_bf16 v[72:75], v[80:83], v[72:75], v[132:135]
	v_mfma_f32_16x16x32_bf16 v[128:131], v[64:67], v[60:63], v[128:131]
	v_mfma_f32_16x16x32_bf16 v[124:127], v[68:71], v[60:63], v[124:127]
	s_add_i32 s23, s3, 0xfffbe000
	buffer_load_dwordx4 v[32:35], v173, s[8:11], s23 offen
	v_mfma_f32_16x16x32_bf16 v[120:123], v[76:79], v[60:63], v[120:123]
	v_mfma_f32_16x16x32_bf16 v[60:63], v[80:83], v[60:63], v[116:119]
	v_mfma_f32_16x16x32_bf16 v[112:115], v[64:67], v[56:59], v[112:115]
	v_mfma_f32_16x16x32_bf16 v[108:111], v[68:71], v[56:59], v[108:111]
	s_add_i32 s15, s3, 0xfffbf000
	buffer_load_dwordx4 v[20:23], v173, s[8:11], s15 offen
	v_mfma_f32_16x16x32_bf16 v[104:107], v[76:79], v[56:59], v[104:107]
	v_mfma_f32_16x16x32_bf16 v[56:59], v[80:83], v[56:59], v[100:103]
	v_mfma_f32_16x16x32_bf16 v[64:67], v[64:67], v[52:55], v[96:99]
	v_mfma_f32_16x16x32_bf16 v[68:71], v[68:71], v[52:55], v[92:95]
	s_add_i32 s23, s3, 0xfffc0000
	buffer_load_dwordx4 v[28:31], v173, s[8:11], s23 offen
	v_mfma_f32_16x16x32_bf16 v[76:79], v[76:79], v[52:55], v[88:91]
	v_mfma_f32_16x16x32_bf16 v[52:55], v[80:83], v[52:55], v[84:87]
	s_waitcnt vmcnt(4)
	v_cvt_pk_bf16_f32 v36, v242, v246
	v_cvt_pk_bf16_f32 v37, v250, v188
	ds_write_b64 v197, v[36:37]
	v_cvt_pk_bf16_f32 v36, v243, v247
	v_cvt_pk_bf16_f32 v37, v251, v189
	ds_write_b64 v198, v[36:37]
	v_cvt_pk_bf16_f32 v36, v244, v248
	v_cvt_pk_bf16_f32 v37, v252, v190
	ds_write_b64 v199, v[36:37]
	v_cvt_pk_bf16_f32 v36, v245, v249
	v_cvt_pk_bf16_f32 v37, v253, v191
	ds_write_b64 v200, v[36:37]
	s_waitcnt lgkmcnt(0)
	s_barrier
	ds_read_b128 v[116:119], v177 offset:0
	s_nop 0
	v_mfma_f32_16x16x32_bf16 v[100:103], v[202:205], v[152:155], v[120:123]
	ds_read_b128 v[120:123], v177 offset:0x2000
	v_mfma_f32_16x16x32_bf16 v[96:99], v[168:171], v[152:155], v[124:127]
	s_mov_b32 m0, s98
	s_add_i32 s15, s14, 0xfff3ff80
	buffer_load_dwordx4 v187, s[4:7], s15 offen lds
	ds_read_b128 v[124:127], v177 offset:0x4000
	v_mfma_f32_16x16x32_bf16 v[92:95], v[164:167], v[152:155], v[128:131]
	ds_read_b128 v[128:131], v177 offset:0x6000
	ds_read_b128 v[132:135], v179 offset:0
	v_mfma_f32_16x16x32_bf16 v[88:91], v[202:205], v[148:151], v[136:139]
	ds_read_b128 v[136:139], v183 offset:0x800
	v_mfma_f32_16x16x32_bf16 v[80:83], v[164:167], v[148:151], v[144:147]
	v_mfma_f32_16x16x32_bf16 v[84:87], v[168:171], v[148:151], v[140:143]
	s_add_i32 m0, s98, 0x2000
	s_add_i32 s23, s14, 0xfff7ff80
	buffer_load_dwordx4 v187, s[4:7], s23 offen lds
	ds_read_b128 v[140:143], v179 offset:0x2000
	ds_read_b128 v[144:147], v183 offset:0x2800
	v_mfma_f32_16x16x32_bf16 v[72:75], v[206:209], v[148:151], v[72:75]
	v_mfma_f32_16x16x32_bf16 v[60:63], v[206:209], v[152:155], v[60:63]
	v_mfma_f32_16x16x32_bf16 v[112:115], v[164:167], v[156:159], v[112:115]
	v_mfma_f32_16x16x32_bf16 v[108:111], v[168:171], v[156:159], v[108:111]
	s_add_i32 m0, s98, 0x4000
	s_add_i32 s15, s14, 0xfffbff80
	buffer_load_dwordx4 v187, s[4:7], s15 offen lds
	v_mfma_f32_16x16x32_bf16 v[104:107], v[202:205], v[156:159], v[104:107]
	v_mfma_f32_16x16x32_bf16 v[56:59], v[206:209], v[156:159], v[56:59]
	v_mfma_f32_16x16x32_bf16 v[64:67], v[164:167], v[160:163], v[64:67]
	v_mfma_f32_16x16x32_bf16 v[68:71], v[168:171], v[160:163], v[68:71]
	s_add_i32 m0, s98, 0x6000
	s_add_i32 s23, s14, 0xffffff80
	buffer_load_dwordx4 v187, s[4:7], s23 offen lds
	v_mfma_f32_16x16x32_bf16 v[76:79], v[202:205], v[160:163], v[76:79]
	v_mfma_f32_16x16x32_bf16 v[52:55], v[206:209], v[160:163], v[52:55]
	ds_read_b128 v[148:151], v181 offset:0
	ds_read_b128 v[152:155], v181 offset:0x2000
	ds_read_b128 v[156:159], v181 offset:0x4000
	ds_read_b128 v[160:163], v181 offset:0x6000
	ds_read_b128 v[164:167], v183 offset:0
	ds_read_b128 v[168:171], v179 offset:0x800
	ds_read_b128 v[202:205], v183 offset:0x2000
	ds_read_b128 v[206:209], v179 offset:0x2800
	s_waitcnt lgkmcnt(8)
	s_nop 0
	v_mfma_f32_16x16x32_bf16 v[80:83], v[132:135], v[116:119], v[80:83]
	v_mfma_f32_16x16x32_bf16 v[84:87], v[136:139], v[116:119], v[84:87]
	s_add_i32 s15, s3, 0xffffd000
	buffer_load_dwordx4 v[242:245], v173, s[8:11], s15 offen
	v_mfma_f32_16x16x32_bf16 v[88:91], v[140:143], v[116:119], v[88:91]
	v_mfma_f32_16x16x32_bf16 v[72:75], v[144:147], v[116:119], v[72:75]
	v_mfma_f32_16x16x32_bf16 v[92:95], v[132:135], v[120:123], v[92:95]
	v_mfma_f32_16x16x32_bf16 v[96:99], v[136:139], v[120:123], v[96:99]
	s_add_i32 s23, s3, 0xffffe000
	buffer_load_dwordx4 v[246:249], v173, s[8:11], s23 offen
	v_mfma_f32_16x16x32_bf16 v[100:103], v[140:143], v[120:123], v[100:103]
	v_mfma_f32_16x16x32_bf16 v[60:63], v[144:147], v[120:123], v[60:63]
	v_mfma_f32_16x16x32_bf16 v[112:115], v[132:135], v[124:127], v[112:115]
	v_mfma_f32_16x16x32_bf16 v[108:111], v[136:139], v[124:127], v[108:111]
	s_add_i32 s15, s3, 0xfffff000
	buffer_load_dwordx4 v[250:253], v173, s[8:11], s15 offen
	v_mfma_f32_16x16x32_bf16 v[104:107], v[140:143], v[124:127], v[104:107]
	v_mfma_f32_16x16x32_bf16 v[56:59], v[144:147], v[124:127], v[56:59]
	v_mfma_f32_16x16x32_bf16 v[64:67], v[132:135], v[128:131], v[64:67]
	v_mfma_f32_16x16x32_bf16 v[68:71], v[136:139], v[128:131], v[68:71]
	buffer_load_dwordx4 v[188:191], v173, s[8:11], s3 offen
	v_mfma_f32_16x16x32_bf16 v[76:79], v[140:143], v[128:131], v[76:79]
	v_mfma_f32_16x16x32_bf16 v[210:213], v[144:147], v[128:131], v[52:55]
	s_waitcnt vmcnt(4)
	v_cvt_pk_bf16_f32 v36, v24, v32
	v_cvt_pk_bf16_f32 v37, v20, v28
	ds_write_b64 v3, v[36:37] offset:49152
	v_cvt_pk_bf16_f32 v36, v25, v33
	v_cvt_pk_bf16_f32 v37, v21, v29
	ds_write_b64 v194, v[36:37] offset:49280
	v_cvt_pk_bf16_f32 v36, v26, v34
	v_cvt_pk_bf16_f32 v37, v22, v30
	ds_write_b64 v195, v[36:37] offset:49408
	v_cvt_pk_bf16_f32 v36, v27, v35
	v_cvt_pk_bf16_f32 v37, v23, v31
	ds_write_b64 v196, v[36:37] offset:49536
	s_waitcnt lgkmcnt(0)
	s_barrier
	s_nop 0
	v_mfma_f32_16x16x32_bf16 v[132:135], v[206:209], v[148:151], v[72:75]
	ds_read_b128 v[72:75], v176 offset:0
	v_mfma_f32_16x16x32_bf16 v[116:119], v[206:209], v[152:155], v[60:63]
	s_mov_b32 m0, s99
	s_add_i32 s15, s14, 0xfff40000
	buffer_load_dwordx4 v187, s[4:7], s15 offen lds
	ds_read_b128 v[60:63], v176 offset:0x2000
	v_mfma_f32_16x16x32_bf16 v[120:123], v[202:205], v[152:155], v[100:103]
	v_mfma_f32_16x16x32_bf16 v[100:103], v[206:209], v[156:159], v[56:59]
	ds_read_b128 v[56:59], v176 offset:0x4000
	ds_read_b128 v[52:55], v176 offset:0x6000
	v_mfma_f32_16x16x32_bf16 v[124:127], v[168:171], v[152:155], v[96:99]
	v_mfma_f32_16x16x32_bf16 v[96:99], v[164:167], v[160:163], v[64:67]
	s_add_i32 m0, s99, 0x2000
	s_add_i32 s23, s14, 0xfff80000
	buffer_load_dwordx4 v187, s[4:7], s23 offen lds
	ds_read_b128 v[64:67], v178 offset:0
	v_mfma_f32_16x16x32_bf16 v[128:131], v[164:167], v[152:155], v[92:95]
	v_mfma_f32_16x16x32_bf16 v[92:95], v[168:171], v[160:163], v[68:71]
	ds_read_b128 v[68:71], v182 offset:0x800
	v_mfma_f32_16x16x32_bf16 v[144:147], v[164:167], v[148:151], v[80:83]
	v_mfma_f32_16x16x32_bf16 v[140:143], v[168:171], v[148:151], v[84:87]
	s_add_i32 m0, s99, 0x4000
	s_add_i32 s15, s14, 0xfffc0000
	buffer_load_dwordx4 v187, s[4:7], s15 offen lds
	v_mfma_f32_16x16x32_bf16 v[136:139], v[202:205], v[148:151], v[88:91]
	v_mfma_f32_16x16x32_bf16 v[112:115], v[164:167], v[156:159], v[112:115]
	v_mfma_f32_16x16x32_bf16 v[108:111], v[168:171], v[156:159], v[108:111]
	v_mfma_f32_16x16x32_bf16 v[104:107], v[202:205], v[156:159], v[104:107]
	s_add_i32 m0, s99, 0x6000
	s_nop 0
	buffer_load_dwordx4 v187, s[4:7], s14 offen lds
	v_mfma_f32_16x16x32_bf16 v[88:91], v[202:205], v[160:163], v[76:79]
	ds_read_b128 v[76:79], v178 offset:0x2000
	ds_read_b128 v[80:83], v182 offset:0x2800
	v_mfma_f32_16x16x32_bf16 v[84:87], v[206:209], v[160:163], v[210:213]
	s_add_i32 s2, s2, 2
	s_add_i32 s3, s3, 0x80000
	s_addk_i32 s14, 0x100
	s_cmp_lt_u32 s2, 27
	s_cbranch_scc1 .LBB0_1340
	ds_read_b128 v[148:151], v180 offset:0
	ds_read_b128 v[152:155], v180 offset:0x2000
	ds_read_b128 v[156:159], v180 offset:0x4000
	ds_read_b128 v[160:163], v180 offset:0x6000
	ds_read_b128 v[164:167], v182 offset:0
	ds_read_b128 v[168:171], v178 offset:0x800
	ds_read_b128 v[202:205], v182 offset:0x2000
	ds_read_b128 v[206:209], v178 offset:0x2800
	s_waitcnt lgkmcnt(8)
	s_nop 0
	v_mfma_f32_16x16x32_bf16 v[144:147], v[64:67], v[72:75], v[144:147]
	v_mfma_f32_16x16x32_bf16 v[140:143], v[68:71], v[72:75], v[140:143]
	v_mfma_f32_16x16x32_bf16 v[136:139], v[76:79], v[72:75], v[136:139]
	v_mfma_f32_16x16x32_bf16 v[72:75], v[80:83], v[72:75], v[132:135]
	v_mfma_f32_16x16x32_bf16 v[128:131], v[64:67], v[60:63], v[128:131]
	v_mfma_f32_16x16x32_bf16 v[124:127], v[68:71], v[60:63], v[124:127]
	v_mfma_f32_16x16x32_bf16 v[120:123], v[76:79], v[60:63], v[120:123]
	v_mfma_f32_16x16x32_bf16 v[60:63], v[80:83], v[60:63], v[116:119]
	v_mfma_f32_16x16x32_bf16 v[112:115], v[64:67], v[56:59], v[112:115]
	v_mfma_f32_16x16x32_bf16 v[108:111], v[68:71], v[56:59], v[108:111]
	v_mfma_f32_16x16x32_bf16 v[104:107], v[76:79], v[56:59], v[104:107]
	v_mfma_f32_16x16x32_bf16 v[100:103], v[80:83], v[56:59], v[100:103]
	v_mfma_f32_16x16x32_bf16 v[96:99], v[64:67], v[52:55], v[96:99]
	v_mfma_f32_16x16x32_bf16 v[116:119], v[68:71], v[52:55], v[92:95]
	v_mfma_f32_16x16x32_bf16 v[132:135], v[76:79], v[52:55], v[88:91]
	v_mfma_f32_16x16x32_bf16 v[210:213], v[80:83], v[52:55], v[84:87]
	s_waitcnt vmcnt(0)
	v_cvt_pk_bf16_f32 v36, v242, v246
	v_cvt_pk_bf16_f32 v37, v250, v188
	ds_write_b64 v197, v[36:37]
	v_cvt_pk_bf16_f32 v36, v243, v247
	v_cvt_pk_bf16_f32 v37, v251, v189
	ds_write_b64 v198, v[36:37]
	v_cvt_pk_bf16_f32 v36, v244, v248
	v_cvt_pk_bf16_f32 v37, v252, v190
	ds_write_b64 v199, v[36:37]
	v_cvt_pk_bf16_f32 v36, v245, v249
	v_cvt_pk_bf16_f32 v37, v253, v191
	ds_write_b64 v200, v[36:37]
	s_waitcnt lgkmcnt(0)
	s_barrier
	s_nop 0
	v_mfma_f32_16x16x32_bf16 v[52:55], v[164:167], v[156:159], v[112:115]
	ds_read_b128 v[112:115], v177 offset:0
	ds_read_b128 v[92:95], v177 offset:0x2000
	ds_read_b128 v[84:87], v177 offset:0x4000
	ds_read_b128 v[76:79], v177 offset:0x6000
	ds_read_b128 v[88:91], v179 offset:0
	v_mfma_f32_16x16x32_bf16 v[68:71], v[164:167], v[160:163], v[96:99]
	ds_read_b128 v[96:99], v183 offset:0x800
	v_mfma_f32_16x16x32_bf16 v[20:23], v[164:167], v[148:151], v[144:147]
	v_mfma_f32_16x16x32_bf16 v[24:27], v[168:171], v[148:151], v[140:143]
	v_mfma_f32_16x16x32_bf16 v[28:31], v[202:205], v[148:151], v[136:139]
	v_mfma_f32_16x16x32_bf16 v[32:35], v[206:209], v[148:151], v[72:75]
	v_mfma_f32_16x16x32_bf16 v[36:39], v[164:167], v[152:155], v[128:131]
	v_mfma_f32_16x16x32_bf16 v[40:43], v[168:171], v[152:155], v[124:127]
	v_mfma_f32_16x16x32_bf16 v[44:47], v[202:205], v[152:155], v[120:123]
	v_mfma_f32_16x16x32_bf16 v[48:51], v[206:209], v[152:155], v[60:63]
	v_mfma_f32_16x16x32_bf16 v[56:59], v[168:171], v[156:159], v[108:111]
	v_mfma_f32_16x16x32_bf16 v[60:63], v[202:205], v[156:159], v[104:107]
	v_mfma_f32_16x16x32_bf16 v[64:67], v[206:209], v[156:159], v[100:103]
	ds_read_b128 v[100:103], v179 offset:0x2000
	ds_read_b128 v[104:107], v183 offset:0x2800
	v_mfma_f32_16x16x32_bf16 v[72:75], v[168:171], v[160:163], v[116:119]
	v_mfma_f32_16x16x32_bf16 v[80:83], v[202:205], v[160:163], v[132:135]
	v_mfma_f32_16x16x32_bf16 v[108:111], v[206:209], v[160:163], v[210:213]
	s_andn2_b64 vcc, exec, s[20:21]
	s_cbranch_vccnz .LBB0_1343
	s_mov_b32 s14, s10
	s_mov_b32 s15, s11
	buffer_load_dwordx4 v[4:7], v173, s[12:15], 0 offen
	buffer_load_dwordx4 v[8:11], v173, s[12:15], s44 offen
	buffer_load_dwordx4 v[12:15], v173, s[12:15], s45 offen
	buffer_load_dwordx4 v[16:19], v173, s[12:15], s46 offen

.LBB0_1415:
	s_cmp_lt_i32 s68, 17
	s_cselect_b64 s[0:1], -1, 0
	s_cmp_gt_i32 s69, 16
	s_cselect_b64 s[2:3], -1, 0
	s_and_b64 s[0:1], s[0:1], s[2:3]
	s_andn2_b64 vcc, exec, s[0:1]
	s_cbranch_vccnz .LBB0_1518
	s_waitcnt vmcnt(0) lgkmcnt(0)
	v_mov_b32_e32 v3, v0
	v_and_b32_e32 v20, 63, v3
	v_lshlrev_b32_e32 v21, 2, v20
	global_load_dword v22, v21, s[94:95] sc1
	s_waitcnt vmcnt(0)
	v_lshlrev_b32_e32 v22, 6, v22
	v_sub_u32_e32 v23, 63, v20
	v_or_b32_e32 v22, v22, v23
	v_mov_b32_e32 v24, 0
	v_readlane_b32 s0, v22, 0
	s_nop 1
	v_cmp_gt_u32_e32 vcc, s0, v22
	s_nop 1
	v_addc_co_u32_e32 v24, vcc, 0, v24, vcc
	v_readlane_b32 s0, v22, 1
	s_nop 1
	v_cmp_gt_u32_e32 vcc, s0, v22
	s_nop 1
	v_addc_co_u32_e32 v24, vcc, 0, v24, vcc
	v_readlane_b32 s0, v22, 2
	s_nop 1
	v_cmp_gt_u32_e32 vcc, s0, v22
	s_nop 1
	v_addc_co_u32_e32 v24, vcc, 0, v24, vcc
	v_readlane_b32 s0, v22, 3
	s_nop 1
	v_cmp_gt_u32_e32 vcc, s0, v22
	s_nop 1
	v_addc_co_u32_e32 v24, vcc, 0, v24, vcc
	v_readlane_b32 s0, v22, 4
	s_nop 1
	v_cmp_gt_u32_e32 vcc, s0, v22
	s_nop 1
	v_addc_co_u32_e32 v24, vcc, 0, v24, vcc
	v_readlane_b32 s0, v22, 5
	s_nop 1
	v_cmp_gt_u32_e32 vcc, s0, v22
	s_nop 1
	v_addc_co_u32_e32 v24, vcc, 0, v24, vcc
	v_readlane_b32 s0, v22, 6
	s_nop 1
	v_cmp_gt_u32_e32 vcc, s0, v22
	s_nop 1
	v_addc_co_u32_e32 v24, vcc, 0, v24, vcc
	v_readlane_b32 s0, v22, 7
	s_nop 1
	v_cmp_gt_u32_e32 vcc, s0, v22
	s_nop 1
	v_addc_co_u32_e32 v24, vcc, 0, v24, vcc
	v_readlane_b32 s0, v22, 8
	s_nop 1
	v_cmp_gt_u32_e32 vcc, s0, v22
	s_nop 1
	v_addc_co_u32_e32 v24, vcc, 0, v24, vcc
	v_readlane_b32 s0, v22, 9
	s_nop 1
	v_cmp_gt_u32_e32 vcc, s0, v22
	s_nop 1
	v_addc_co_u32_e32 v24, vcc, 0, v24, vcc
	v_readlane_b32 s0, v22, 10
	s_nop 1
	v_cmp_gt_u32_e32 vcc, s0, v22
	s_nop 1
	v_addc_co_u32_e32 v24, vcc, 0, v24, vcc
	v_readlane_b32 s0, v22, 11
	s_nop 1
	v_cmp_gt_u32_e32 vcc, s0, v22
	s_nop 1
	v_addc_co_u32_e32 v24, vcc, 0, v24, vcc
	v_readlane_b32 s0, v22, 12
	s_nop 1
	v_cmp_gt_u32_e32 vcc, s0, v22
	s_nop 1
	v_addc_co_u32_e32 v24, vcc, 0, v24, vcc
	v_readlane_b32 s0, v22, 13
	s_nop 1
	v_cmp_gt_u32_e32 vcc, s0, v22
	s_nop 1
	v_addc_co_u32_e32 v24, vcc, 0, v24, vcc
	v_readlane_b32 s0, v22, 14
	s_nop 1
	v_cmp_gt_u32_e32 vcc, s0, v22
	s_nop 1
	v_addc_co_u32_e32 v24, vcc, 0, v24, vcc
	v_readlane_b32 s0, v22, 15
	s_nop 1
	v_cmp_gt_u32_e32 vcc, s0, v22
	s_nop 1
	v_addc_co_u32_e32 v24, vcc, 0, v24, vcc
	v_readlane_b32 s0, v22, 16
	s_nop 1
	v_cmp_gt_u32_e32 vcc, s0, v22
	s_nop 1
	v_addc_co_u32_e32 v24, vcc, 0, v24, vcc
	v_readlane_b32 s0, v22, 17
	s_nop 1
	v_cmp_gt_u32_e32 vcc, s0, v22
	s_nop 1
	v_addc_co_u32_e32 v24, vcc, 0, v24, vcc
	v_readlane_b32 s0, v22, 18
	s_nop 1
	v_cmp_gt_u32_e32 vcc, s0, v22
	s_nop 1
	v_addc_co_u32_e32 v24, vcc, 0, v24, vcc
	v_readlane_b32 s0, v22, 19
	s_nop 1
	v_cmp_gt_u32_e32 vcc, s0, v22
	s_nop 1
	v_addc_co_u32_e32 v24, vcc, 0, v24, vcc
	v_readlane_b32 s0, v22, 20
	s_nop 1
	v_cmp_gt_u32_e32 vcc, s0, v22
	s_nop 1
	v_addc_co_u32_e32 v24, vcc, 0, v24, vcc
	v_readlane_b32 s0, v22, 21
	s_nop 1
	v_cmp_gt_u32_e32 vcc, s0, v22
	s_nop 1
	v_addc_co_u32_e32 v24, vcc, 0, v24, vcc
	v_readlane_b32 s0, v22, 22
	s_nop 1
	v_cmp_gt_u32_e32 vcc, s0, v22
	s_nop 1
	v_addc_co_u32_e32 v24, vcc, 0, v24, vcc
	v_readlane_b32 s0, v22, 23
	s_nop 1
	v_cmp_gt_u32_e32 vcc, s0, v22
	s_nop 1
	v_addc_co_u32_e32 v24, vcc, 0, v24, vcc
	v_readlane_b32 s0, v22, 24
	s_nop 1
	v_cmp_gt_u32_e32 vcc, s0, v22
	s_nop 1
	v_addc_co_u32_e32 v24, vcc, 0, v24, vcc
	v_readlane_b32 s0, v22, 25
	s_nop 1
	v_cmp_gt_u32_e32 vcc, s0, v22
	s_nop 1
	v_addc_co_u32_e32 v24, vcc, 0, v24, vcc
	v_readlane_b32 s0, v22, 26
	s_nop 1
	v_cmp_gt_u32_e32 vcc, s0, v22
	s_nop 1
	v_addc_co_u32_e32 v24, vcc, 0, v24, vcc
	v_readlane_b32 s0, v22, 27
	s_nop 1
	v_cmp_gt_u32_e32 vcc, s0, v22
	s_nop 1
	v_addc_co_u32_e32 v24, vcc, 0, v24, vcc
	v_readlane_b32 s0, v22, 28
	s_nop 1
	v_cmp_gt_u32_e32 vcc, s0, v22
	s_nop 1
	v_addc_co_u32_e32 v24, vcc, 0, v24, vcc
	v_readlane_b32 s0, v22, 29
	s_nop 1
	v_cmp_gt_u32_e32 vcc, s0, v22
	s_nop 1
	v_addc_co_u32_e32 v24, vcc, 0, v24, vcc
	v_readlane_b32 s0, v22, 30
	s_nop 1
	v_cmp_gt_u32_e32 vcc, s0, v22
	s_nop 1
	v_addc_co_u32_e32 v24, vcc, 0, v24, vcc
	v_readlane_b32 s0, v22, 31
	s_nop 1
	v_cmp_gt_u32_e32 vcc, s0, v22
	s_nop 1
	v_addc_co_u32_e32 v24, vcc, 0, v24, vcc
	v_readlane_b32 s0, v22, 32
	s_nop 1
	v_cmp_gt_u32_e32 vcc, s0, v22
	s_nop 1
	v_addc_co_u32_e32 v24, vcc, 0, v24, vcc
	v_readlane_b32 s0, v22, 33
	s_nop 1
	v_cmp_gt_u32_e32 vcc, s0, v22
	s_nop 1
	v_addc_co_u32_e32 v24, vcc, 0, v24, vcc
	v_readlane_b32 s0, v22, 34
	s_nop 1
	v_cmp_gt_u32_e32 vcc, s0, v22
	s_nop 1
	v_addc_co_u32_e32 v24, vcc, 0, v24, vcc
	v_readlane_b32 s0, v22, 35
	s_nop 1
	v_cmp_gt_u32_e32 vcc, s0, v22
	s_nop 1
	v_addc_co_u32_e32 v24, vcc, 0, v24, vcc
	v_readlane_b32 s0, v22, 36
	s_nop 1
	v_cmp_gt_u32_e32 vcc, s0, v22
	s_nop 1
	v_addc_co_u32_e32 v24, vcc, 0, v24, vcc
	v_readlane_b32 s0, v22, 37
	s_nop 1
	v_cmp_gt_u32_e32 vcc, s0, v22
	s_nop 1
	v_addc_co_u32_e32 v24, vcc, 0, v24, vcc
	v_readlane_b32 s0, v22, 38
	s_nop 1
	v_cmp_gt_u32_e32 vcc, s0, v22
	s_nop 1
	v_addc_co_u32_e32 v24, vcc, 0, v24, vcc
	v_readlane_b32 s0, v22, 39
	s_nop 1
	v_cmp_gt_u32_e32 vcc, s0, v22
	s_nop 1
	v_addc_co_u32_e32 v24, vcc, 0, v24, vcc
	v_readlane_b32 s0, v22, 40
	s_nop 1
	v_cmp_gt_u32_e32 vcc, s0, v22
	s_nop 1
	v_addc_co_u32_e32 v24, vcc, 0, v24, vcc
	v_readlane_b32 s0, v22, 41
	s_nop 1
	v_cmp_gt_u32_e32 vcc, s0, v22
	s_nop 1
	v_addc_co_u32_e32 v24, vcc, 0, v24, vcc
	v_readlane_b32 s0, v22, 42
	s_nop 1
	v_cmp_gt_u32_e32 vcc, s0, v22
	s_nop 1
	v_addc_co_u32_e32 v24, vcc, 0, v24, vcc
	v_readlane_b32 s0, v22, 43
	s_nop 1
	v_cmp_gt_u32_e32 vcc, s0, v22
	s_nop 1
	v_addc_co_u32_e32 v24, vcc, 0, v24, vcc
	v_readlane_b32 s0, v22, 44
	s_nop 1
	v_cmp_gt_u32_e32 vcc, s0, v22
	s_nop 1
	v_addc_co_u32_e32 v24, vcc, 0, v24, vcc
	v_readlane_b32 s0, v22, 45
	s_nop 1
	v_cmp_gt_u32_e32 vcc, s0, v22
	s_nop 1
	v_addc_co_u32_e32 v24, vcc, 0, v24, vcc
	v_readlane_b32 s0, v22, 46
	s_nop 1
	v_cmp_gt_u32_e32 vcc, s0, v22
	s_nop 1
	v_addc_co_u32_e32 v24, vcc, 0, v24, vcc
	v_readlane_b32 s0, v22, 47
	s_nop 1
	v_cmp_gt_u32_e32 vcc, s0, v22
	s_nop 1
	v_addc_co_u32_e32 v24, vcc, 0, v24, vcc
	v_readlane_b32 s0, v22, 48
	s_nop 1
	v_cmp_gt_u32_e32 vcc, s0, v22
	s_nop 1
	v_addc_co_u32_e32 v24, vcc, 0, v24, vcc
	v_readlane_b32 s0, v22, 49
	s_nop 1
	v_cmp_gt_u32_e32 vcc, s0, v22
	s_nop 1
	v_addc_co_u32_e32 v24, vcc, 0, v24, vcc
	v_readlane_b32 s0, v22, 50
	s_nop 1
	v_cmp_gt_u32_e32 vcc, s0, v22
	s_nop 1
	v_addc_co_u32_e32 v24, vcc, 0, v24, vcc
	v_readlane_b32 s0, v22, 51
	s_nop 1
	v_cmp_gt_u32_e32 vcc, s0, v22
	s_nop 1
	v_addc_co_u32_e32 v24, vcc, 0, v24, vcc
	v_readlane_b32 s0, v22, 52
	s_nop 1
	v_cmp_gt_u32_e32 vcc, s0, v22
	s_nop 1
	v_addc_co_u32_e32 v24, vcc, 0, v24, vcc
	v_readlane_b32 s0, v22, 53
	s_nop 1
	v_cmp_gt_u32_e32 vcc, s0, v22
	s_nop 1
	v_addc_co_u32_e32 v24, vcc, 0, v24, vcc
	v_readlane_b32 s0, v22, 54
	s_nop 1
	v_cmp_gt_u32_e32 vcc, s0, v22
	s_nop 1
	v_addc_co_u32_e32 v24, vcc, 0, v24, vcc
	v_readlane_b32 s0, v22, 55
	s_nop 1
	v_cmp_gt_u32_e32 vcc, s0, v22
	s_nop 1
	v_addc_co_u32_e32 v24, vcc, 0, v24, vcc
	v_readlane_b32 s0, v22, 56
	s_nop 1
	v_cmp_gt_u32_e32 vcc, s0, v22
	s_nop 1
	v_addc_co_u32_e32 v24, vcc, 0, v24, vcc
	v_readlane_b32 s0, v22, 57
	s_nop 1
	v_cmp_gt_u32_e32 vcc, s0, v22
	s_nop 1
	v_addc_co_u32_e32 v24, vcc, 0, v24, vcc
	v_readlane_b32 s0, v22, 58
	s_nop 1
	v_cmp_gt_u32_e32 vcc, s0, v22
	s_nop 1
	v_addc_co_u32_e32 v24, vcc, 0, v24, vcc
	v_readlane_b32 s0, v22, 59
	s_nop 1
	v_cmp_gt_u32_e32 vcc, s0, v22
	s_nop 1
	v_addc_co_u32_e32 v24, vcc, 0, v24, vcc
	v_readlane_b32 s0, v22, 60
	s_nop 1
	v_cmp_gt_u32_e32 vcc, s0, v22
	s_nop 1
	v_addc_co_u32_e32 v24, vcc, 0, v24, vcc
	v_readlane_b32 s0, v22, 61
	s_nop 1
	v_cmp_gt_u32_e32 vcc, s0, v22
	s_nop 1
	v_addc_co_u32_e32 v24, vcc, 0, v24, vcc
	v_readlane_b32 s0, v22, 62
	s_nop 1
	v_cmp_gt_u32_e32 vcc, s0, v22
	s_nop 1
	v_addc_co_u32_e32 v24, vcc, 0, v24, vcc
	v_readlane_b32 s0, v22, 63
	s_nop 1
	v_cmp_gt_u32_e32 vcc, s0, v22
	s_nop 1
	v_addc_co_u32_e32 v24, vcc, 0, v24, vcc
	s_lshr_b32 s1, s65, 4
	v_cmp_eq_u32_e32 vcc, s1, v24
	s_nop 3
	s_ff1_i32_b64 s100, vcc
	s_sub_i32 s2, 31, s1
	v_cmp_eq_u32_e32 vcc, s2, v24
	s_nop 3
	s_ff1_i32_b64 s0, vcc
	s_lshl_b32 s0, s0, 8
	s_or_b32 s100, s100, s0
	s_add_i32 s2, s1, 32
	v_cmp_eq_u32_e32 vcc, s2, v24
	s_nop 3
	s_ff1_i32_b64 s0, vcc
	s_lshl_b32 s0, s0, 16
	s_or_b32 s100, s100, s0
	s_sub_i32 s2, 63, s1
	v_cmp_eq_u32_e32 vcc, s2, v24
	s_nop 3
	s_ff1_i32_b64 s0, vcc
	s_lshl_b32 s0, s0, 24
	s_or_b32 s100, s100, s0
	s_cmpk_gt_i32 s65, 0x3ff
	v_and_b32_e32 v2, 15, v3
	v_mul_lo_u32 v1, v2, s33
	v_add_u32_e32 v1, s65, v1
	v_lshrrev_b32_e32 v1, 2, v1
	v_and_b32_e32 v4, 0xfc, v1
	v_and_b32_e32 v20, 3, v2
	v_lshlrev_b32_e32 v20, 3, v20
	v_lshrrev_b32_e64 v4, v20, s100
	v_and_b32_e32 v4, 0xff, v4
	v_lshlrev_b32_e32 v4, 2, v4
	global_load_dword v1, v4, s[94:95] sc1
	global_load_dword v172, v4, s[94:95] offset:256 sc1
	s_cbranch_scc1 .LBB0_1464
	s_add_u32 s24, s94, 0x4b000000
	s_addc_u32 s25, s95, 0
	s_add_u32 s0, s94, 0x4f000000
	v_readlane_b32 s2, v254, 0
	s_addc_u32 s1, s95, 0
	v_bfe_u32 v4, v3, 4, 2
	s_lshr_b32 s2, s2, 8
	v_lshlrev_b32_e32 v5, 4, v2
	v_lshlrev_b32_e32 v6, 4, v3
	s_lshl_b32 s3, s2, 1
	v_lshl_or_b32 v173, v4, 15, v5
	v_ashrrev_i32_e32 v5, 3, v3
	v_and_b32_e32 v6, 0x70, v6
	s_add_i32 s3, s3, s97
	v_lshl_or_b32 v174, v5, 11, v6
	v_lshlrev_b32_e32 v6, 7, v5
	v_xor_b32_e32 v5, v5, v3
	v_bfe_u32 v175, v3, 5, 1
	v_and_b32_e32 v10, 7, v3
	v_lshlrev_b32_e32 v11, 2, v3
	v_bitop3_b32 v3, v4, v3, 7 bitop3:0x78
	v_lshrrev_b32_e32 v13, 2, v2
	s_and_b32 s26, s3, 3
	v_xor_b32_e32 v13, v3, v13
	v_lshlrev_b32_e32 v12, 7, v2
	s_lshl_b32 s3, s26, 11
	s_lshl_b32 s4, s2, 13
	v_lshlrev_b32_e32 v13, 4, v13
	v_lshl_add_u32 v3, v3, 4, 0
	v_lshlrev_b32_e32 v5, 4, v5
	v_lshlrev_b32_e32 v8, 3, v4
	v_add3_u32 v176, v3, v12, s3
	v_or3_b32 v3, v13, s4, v12
	v_and_b32_e32 v5, 0x70, v5
	v_lshlrev_b32_e32 v7, 9, v2
	v_bitop3_b32 v4, v4, v10, 4 bitop3:0x36
	s_add_i32 s5, s4, 0xc000
	v_add_u32_e32 v3, 0, v3
	v_lshl_or_b32 v191, v2, 12, v8
	v_mov_b32_e32 v2, 0
	v_and_b32_e32 v9, 8, v8
	v_or3_b32 v14, v13, s5, v12
	v_add_u32_e32 v178, 0xc000, v3
	v_add_u32_e32 v179, 0x1c000, v3
	v_lshl_add_u32 v3, v4, 4, 0
	v_add3_u32 v184, 0, v5, v6
	v_mov_b32_e32 v4, v2
	v_mov_b32_e32 v5, v2
	v_add3_u32 v180, v3, v12, s3
	v_xad_u32 v182, v14, 64, 0
	v_add3_u32 v185, 0, v7, v9
	v_bitop3_b32 v192, v11, v10, 4 bitop3:0x6c
	v_mov_b32_e32 v3, v2
	v_mbcnt_lo_u32_b32 v6, -1, 0
	v_mov_b64_e32 v[18:19], v[4:5]
	v_mov_b64_e32 v[14:15], v[4:5]
	v_mov_b64_e32 v[10:11], v[4:5]
	s_mov_b32 s7, 0x20000
	s_or_b32 s30, s26, 4
	s_or_b32 s34, s26, 8
	s_or_b32 s36, s26, 12
	s_or_b32 s38, s26, 16
	v_mbcnt_hi_u32_b32 v193, -1, v6
	v_mov_b64_e32 v[16:17], v[2:3]
	v_mov_b64_e32 v[12:13], v[2:3]
	v_mov_b64_e32 v[8:9], v[2:3]
	v_mov_b64_e32 v[6:7], v[4:5]
	s_mov_b32 s27, 0
	v_add_u32_e32 v177, 0x10000, v176
	v_add_u32_e32 v181, 0x10000, v180
	v_add_u32_e32 v183, 0x10000, v182
	v_add_u32_e32 v186, 0x10000, v184
	v_add_u32_e32 v187, 0x12000, v184
	v_add_u32_e32 v188, 0x14000, v184
	v_add_u32_e32 v189, 0x16000, v184
	v_add_u32_e32 v190, 0x18000, v184
	s_and_b32 s1, s1, 0xffff
	s_brev_b32 s10, -2
	s_mov_b32 s11, s7
	s_lshl_b32 s28, s26, 15
	s_lshl_b32 s29, s2, 7
	s_lshl_b32 s31, s30, 15
	s_lshl_b32 s35, s34, 15
	s_lshl_b32 s37, s36, 15
	s_lshl_b32 s39, s38, 15
	s_mov_b64 s[16:17], 0
	s_mov_b32 s40, 0x40000
	s_mov_b32 s41, 0x60000
	s_mov_b32 s42, 0x80000
	s_movk_i32 s43, 0x2000
	s_movk_i32 s44, 0x4000
	s_movk_i32 s45, 0x6000
	s_movk_i32 s46, 0x80
	s_mov_b32 s47, 0x20080
	s_mov_b32 s48, 0x40080
	s_mov_b32 s49, 0x60080
	s_mov_b32 s50, 0x80080
	s_mov_b32 s51, 0x82000
	s_mov_b32 s52, 0x84000
	s_mov_b32 s53, 0x86000
	v_mov_b64_e32 v[4:5], v[2:3]
	s_branch .LBB0_1419

.LBB0_1424:
	s_add_i32 s56, s65, s33
	s_cmpk_lt_i32 s56, 0x400
	s_cselect_b64 s[20:21], -1, 0
	s_cmpk_gt_i32 s56, 0x3ff
	s_cselect_b64 s[18:19], -1, 0
	s_cmp_lt_i32 s54, 1
	s_cbranch_scc1 .LBB0_1463
	s_lshl_b32 s3, s65, 7
	s_and_b32 s57, s3, 0x780
	s_add_i32 s3, s27, 1
	s_and_b32 s3, s3, 3
	s_lshl_b32 s3, s3, 3
	s_lshr_b32 s3, s100, s3
	s_and_b32 s3, s3, 0xff
	s_lshl_b32 s3, s3, 23
	s_add_u32 s4, s88, s3
	s_addc_u32 s5, s89, 0
	s_ashr_i32 s3, s2, 31
	s_lshl_b64 s[2:3], s[2:3], 23
	s_add_u32 s2, s88, s2
	s_addc_u32 s3, s89, s3
	s_and_b32 s6, s97, 1
	s_lshl_b32 s12, s6, 8
	s_add_u32 s2, s2, s12
	s_addc_u32 s3, s3, 0
	s_lshl_b32 s8, s57, 2
	s_add_u32 s8, s2, s8
	s_addc_u32 s9, s3, 0
	s_lshl_b32 s2, s97, 3
	s_and_b32 s2, s2, -16
	s_ashr_i32 s3, s2, 31
	s_lshl_b64 s[2:3], s[2:3], 13
	s_add_u32 s8, s8, s2
	s_addc_u32 s9, s9, s3
	s_and_b32 s9, s9, 0xffff
	s_and_b32 s13, s97, 0xffffffe
	s_add_u32 s4, s4, s12
	v_lshl_add_u32 v20, s6, 13, v185
	s_addc_u32 s5, s5, 0
	s_lshl_b32 s6, s56, 9
	s_and_b32 s6, s6, 0x1e00
	s_add_u32 s4, s4, s6
	v_bitop3_b32 v3, s13, v192, v175 bitop3:0x36
	s_addc_u32 s5, s5, 0
	v_lshlrev_b32_e32 v21, 4, v3
	s_add_u32 s12, s4, s2
	v_add_u32_e32 v3, v20, v21
	v_xad_u32 v194, v21, 16, v20
	v_xad_u32 v195, v21, 32, v20
	v_xad_u32 v196, v21, 48, v20
	s_addc_u32 s2, s5, s3
	v_add_u32_e32 v197, 0x1c000, v3
	v_add_u32_e32 v198, 0x1c080, v194
	v_add_u32_e32 v199, 0x1c100, v195
	v_add_u32_e32 v200, 0x1c180, v196
	s_and_b32 s13, s2, 0xffff
	s_or_b32 s58, s57, 16
	s_or_b32 s59, s57, 32
	s_or_b32 s62, s57, 48
	s_mov_b32 s63, 0

	.amdhsa_kernel _Z6mk_fwd4Args
		.amdhsa_group_segment_fixed_size 0
		.amdhsa_private_segment_fixed_size 0
		.amdhsa_kernarg_size 560
		.amdhsa_user_sgpr_count 2
		.amdhsa_user_sgpr_dispatch_ptr 0
		.amdhsa_user_sgpr_queue_ptr 0
		.amdhsa_user_sgpr_kernarg_segment_ptr 1
		.amdhsa_user_sgpr_dispatch_id 0
		.amdhsa_user_sgpr_kernarg_preload_length 0
		.amdhsa_user_sgpr_kernarg_preload_offset 0
		.amdhsa_user_sgpr_private_segment_size 0
		.amdhsa_uses_dynamic_stack 0
		.amdhsa_enable_private_segment 0
		.amdhsa_system_sgpr_workgroup_id_x 1
		.amdhsa_system_sgpr_workgroup_id_y 0
		.amdhsa_system_sgpr_workgroup_id_z 0
		.amdhsa_system_sgpr_workgroup_info 0
		.amdhsa_system_vgpr_workitem_id 0
		.amdhsa_next_free_vgpr 256
		.amdhsa_next_free_sgpr 102
		.amdhsa_accum_offset 256
		.amdhsa_reserve_vcc 1
		.amdhsa_float_round_mode_32 0
		.amdhsa_float_round_mode_16_64 0
		.amdhsa_float_denorm_mode_32 3
		.amdhsa_float_denorm_mode_16_64 3
		.amdhsa_dx10_clamp 1
		.amdhsa_ieee_mode 1
		.amdhsa_fp16_overflow 0
		.amdhsa_tg_split 0
		.amdhsa_exception_fp_ieee_invalid_op 0
		.amdhsa_exception_fp_denorm_src 0
		.amdhsa_exception_fp_ieee_div_zero 0
		.amdhsa_exception_fp_ieee_overflow 0
		.amdhsa_exception_fp_ieee_underflow 0
		.amdhsa_exception_fp_ieee_inexact 0
		.amdhsa_exception_int_div_zero 0
	.end_amdhsa_kernel

.Lfunc_end0:
	.size	_Z6mk_fwd4Args, .Lfunc_end0-_Z6mk_fwd4Args
	.set _Z6mk_fwd4Args.num_vgpr, 256
	.set _Z6mk_fwd4Args.num_agpr, 0
	.set _Z6mk_fwd4Args.numbered_sgpr, 102
	.set _Z6mk_fwd4Args.num_named_barrier, 0
	.set _Z6mk_fwd4Args.private_seg_size, 0
	.set _Z6mk_fwd4Args.uses_vcc, 1
	.set _Z6mk_fwd4Args.uses_flat_scratch, 0
	.set _Z6mk_fwd4Args.has_dyn_sized_stack, 0
	.set _Z6mk_fwd4Args.has_recursion, 0
	.set _Z6mk_fwd4Args.has_indirect_call, 0

amdhsa.kernels:
  - .agpr_count:     0
    .args:
      - .offset:         0
        .size:           304
        .value_kind:     by_value
      - .offset:         304
        .size:           4
        .value_kind:     hidden_block_count_x
      - .offset:         308
        .size:           4
        .value_kind:     hidden_block_count_y
      - .offset:         312
        .size:           4
        .value_kind:     hidden_block_count_z
      - .offset:         316
        .size:           2
        .value_kind:     hidden_group_size_x
      - .offset:         318
        .size:           2
        .value_kind:     hidden_group_size_y
      - .offset:         320
        .size:           2
        .value_kind:     hidden_group_size_z
      - .offset:         322
        .size:           2
        .value_kind:     hidden_remainder_x
      - .offset:         324
        .size:           2
        .value_kind:     hidden_remainder_y
      - .offset:         326
        .size:           2
        .value_kind:     hidden_remainder_z
      - .offset:         344
        .size:           8
        .value_kind:     hidden_global_offset_x
      - .offset:         352
        .size:           8
        .value_kind:     hidden_global_offset_y
      - .offset:         360
        .size:           8
        .value_kind:     hidden_global_offset_z
      - .offset:         368
        .size:           2
        .value_kind:     hidden_grid_dims
      - .offset:         424
        .size:           4
        .value_kind:     hidden_dynamic_lds_size
    .group_segment_fixed_size: 0
    .kernarg_segment_align: 8
    .kernarg_segment_size: 560
    .language:       OpenCL C
    .language_version:
      - 2
      - 0
    .max_flat_workgroup_size: 512
    .name:           _Z6mk_fwd4Args
    .private_segment_fixed_size: 0
    .sgpr_count:     108
    .sgpr_spill_count: 122
    .symbol:         _Z6mk_fwd4Args.kd
    .uniform_work_group_size: 1
    .uses_dynamic_stack: false
    .vgpr_count:     256
    .vgpr_spill_count: 0
    .wavefront_size: 64
  - .agpr_count:     0
    .args:
      - .address_space:  global
        .offset:         0
        .size:           8
        .value_kind:     global_buffer
      - .offset:         8
        .size:           4
        .value_kind:     by_value
      - .offset:         12
        .size:           4
        .value_kind:     by_value
      - .address_space:  global
        .offset:         16
        .size:           8
        .value_kind:     global_buffer
      - .offset:         24
        .size:           4
        .value_kind:     by_value
      - .offset:         28
        .size:           4
        .value_kind:     by_value
      - .offset:         32
        .size:           8
        .value_kind:     by_value
      - .offset:         40
        .size:           4
        .value_kind:     by_value
    .group_segment_fixed_size: 4224
    .kernarg_segment_align: 8
    .kernarg_segment_size: 44
    .language:       OpenCL C
    .language_version:
      - 2
      - 0
    .max_flat_workgroup_size: 1024
    .name:           _Z11k_transposePKfiiPtiimi
    .private_segment_fixed_size: 0
    .sgpr_count:     20
    .sgpr_spill_count: 0
    .symbol:         _Z11k_transposePKfiiPtiimi.kd
    .uniform_work_group_size: 1
    .uses_dynamic_stack: false
    .vgpr_count:     16
    .vgpr_spill_count: 0
    .wavefront_size: 64
  - .agpr_count:     0
    .args:
      - .address_space:  global
        .offset:         0
        .size:           8
        .value_kind:     global_buffer
      - .address_space:  global
        .offset:         8
        .size:           8
        .value_kind:     global_buffer
      - .offset:         16
        .size:           4
        .value_kind:     hidden_block_count_x
      - .offset:         20
        .size:           4
        .value_kind:     hidden_block_count_y
      - .offset:         24
        .size:           4
        .value_kind:     hidden_block_count_z
      - .offset:         28
        .size:           2
        .value_kind:     hidden_group_size_x
      - .offset:         30
        .size:           2
        .value_kind:     hidden_group_size_y
      - .offset:         32
        .size:           2
        .value_kind:     hidden_group_size_z
      - .offset:         34
        .size:           2
        .value_kind:     hidden_remainder_x
      - .offset:         36
        .size:           2
        .value_kind:     hidden_remainder_y
      - .offset:         38
        .size:           2
        .value_kind:     hidden_remainder_z
      - .offset:         56
        .size:           8
        .value_kind:     hidden_global_offset_x
      - .offset:         64
        .size:           8
        .value_kind:     hidden_global_offset_y
      - .offset:         72
        .size:           8
        .value_kind:     hidden_global_offset_z
      - .offset:         80
        .size:           2
        .value_kind:     hidden_grid_dims
    .group_segment_fixed_size: 0
    .kernarg_segment_align: 8
    .kernarg_segment_size: 272
    .language:       OpenCL C
    .language_version:
      - 2
      - 0
    .max_flat_workgroup_size: 1024
    .name:           _Z6k_wqbhPKfPt
    .private_segment_fixed_size: 0
    .sgpr_count:     14
    .sgpr_spill_count: 0
    .symbol:         _Z6k_wqbhPKfPt.kd
    .uniform_work_group_size: 1
    .uses_dynamic_stack: false
    .vgpr_count:     9
    .vgpr_spill_count: 0
    .wavefront_size: 64
  - .agpr_count:     0
    .args:
      - .address_space:  global
        .offset:         0
        .size:           8
        .value_kind:     global_buffer
      - .address_space:  global
        .offset:         8
        .size:           8
        .value_kind:     global_buffer
      - .address_space:  global
        .offset:         16
        .size:           8
        .value_kind:     global_buffer
    .group_segment_fixed_size: 16
    .kernarg_segment_align: 8
    .kernarg_segment_size: 24
    .language:       OpenCL C
    .language_version:
      - 2
      - 0
    .max_flat_workgroup_size: 1024
    .name:           _Z14k_rmsnorm_bf16PKfS0_Pt
    .private_segment_fixed_size: 0
    .sgpr_count:     16
    .sgpr_spill_count: 0
    .symbol:         _Z14k_rmsnorm_bf16PKfS0_Pt.kd
    .uniform_work_group_size: 1
    .uses_dynamic_stack: false
    .vgpr_count:     22
    .vgpr_spill_count: 0
    .wavefront_size: 64
  - .agpr_count:     0
    .args:
      - .address_space:  global
        .offset:         0
        .size:           8
        .value_kind:     global_buffer
      - .address_space:  global
        .offset:         8
        .size:           8
        .value_kind:     global_buffer
      - .offset:         16
        .size:           4
        .value_kind:     hidden_block_count_x
      - .offset:         20
        .size:           4
        .value_kind:     hidden_block_count_y
      - .offset:         24
        .size:           4
        .value_kind:     hidden_block_count_z
      - .offset:         28
        .size:           2
        .value_kind:     hidden_group_size_x
      - .offset:         30
        .size:           2
        .value_kind:     hidden_group_size_y
      - .offset:         32
        .size:           2
        .value_kind:     hidden_group_size_z
      - .offset:         34
        .size:           2
        .value_kind:     hidden_remainder_x
      - .offset:         36
        .size:           2
        .value_kind:     hidden_remainder_y
      - .offset:         38
        .size:           2
        .value_kind:     hidden_remainder_z
      - .offset:         56
        .size:           8
        .value_kind:     hidden_global_offset_x
      - .offset:         64
        .size:           8
        .value_kind:     hidden_global_offset_y
      - .offset:         72
        .size:           8
        .value_kind:     hidden_global_offset_z
      - .offset:         80
        .size:           2
        .value_kind:     hidden_grid_dims
    .group_segment_fixed_size: 0
    .kernarg_segment_align: 8
    .kernarg_segment_size: 272
    .language:       OpenCL C
    .language_version:
      - 2
      - 0
    .max_flat_workgroup_size: 1024
    .name:           _Z12k_rope_tablePKiPf
    .private_segment_fixed_size: 0
    .sgpr_count:     17
    .sgpr_spill_count: 0
    .symbol:         _Z12k_rope_tablePKiPf.kd
    .uniform_work_group_size: 1
    .uses_dynamic_stack: false
    .vgpr_count:     34
    .vgpr_spill_count: 0
    .wavefront_size: 64
  - .agpr_count:     0
    .args:
      - .address_space:  global
        .offset:         0
        .size:           8
        .value_kind:     global_buffer
      - .address_space:  global
        .offset:         8
        .size:           8
        .value_kind:     global_buffer
      - .address_space:  global
        .offset:         16
        .size:           8
        .value_kind:     global_buffer
      - .address_space:  global
        .offset:         24
        .size:           8
        .value_kind:     global_buffer
    .group_segment_fixed_size: 0
    .kernarg_segment_align: 8
    .kernarg_segment_size: 32
    .language:       OpenCL C
    .language_version:
      - 2
      - 0
    .max_flat_workgroup_size: 1024
    .name:           _Z12k_rope_applyPKfS0_PtS1_
    .private_segment_fixed_size: 0
    .sgpr_count:     22
    .sgpr_spill_count: 0
    .symbol:         _Z12k_rope_applyPKfS0_PtS1_.kd
    .uniform_work_group_size: 1
    .uses_dynamic_stack: false
    .vgpr_count:     19
    .vgpr_spill_count: 0
    .wavefront_size: 64
  - .agpr_count:     0
    .args:
      - .address_space:  global
        .offset:         0
        .size:           8
        .value_kind:     global_buffer
      - .offset:         8
        .size:           72
        .value_kind:     by_value
      - .address_space:  global
        .offset:         80
        .size:           8
        .value_kind:     global_buffer
      - .address_space:  global
        .offset:         88
        .size:           8
        .value_kind:     global_buffer
    .group_segment_fixed_size: 1024
    .kernarg_segment_align: 8
    .kernarg_segment_size: 96
    .language:       OpenCL C
    .language_version:
      - 2
      - 0
    .max_flat_workgroup_size: 256
    .name:           _Z6k_prepPKt5PrepWPfS2_
    .private_segment_fixed_size: 0
    .sgpr_count:     36
    .sgpr_spill_count: 0
    .symbol:         _Z6k_prepPKt5PrepWPfS2_.kd
    .uniform_work_group_size: 1
    .uses_dynamic_stack: false
    .vgpr_count:     63
    .vgpr_spill_count: 0
    .wavefront_size: 64
  - .agpr_count:     0
    .args:
      - .address_space:  global
        .offset:         0
        .size:           8
        .value_kind:     global_buffer
      - .address_space:  global
        .offset:         8
        .size:           8
        .value_kind:     global_buffer
    .group_segment_fixed_size: 0
    .kernarg_segment_align: 8
    .kernarg_segment_size: 16
    .language:       OpenCL C
    .language_version:
      - 2
      - 0
    .max_flat_workgroup_size: 256
    .name:           _Z6k_scanPKfPf
    .private_segment_fixed_size: 0
    .sgpr_count:     14
    .sgpr_spill_count: 0
    .symbol:         _Z6k_scanPKfPf.kd
    .uniform_work_group_size: 1
    .uses_dynamic_stack: false
    .vgpr_count:     29
    .vgpr_spill_count: 0
    .wavefront_size: 64
  - .agpr_count:     0
    .args:
      - .address_space:  global
        .offset:         0
        .size:           8
        .value_kind:     global_buffer
      - .address_space:  global
        .offset:         8
        .size:           8
        .value_kind:     global_buffer
      - .address_space:  global
        .offset:         16
        .size:           8
        .value_kind:     global_buffer
      - .address_space:  global
        .offset:         24
        .size:           8
        .value_kind:     global_buffer
      - .address_space:  global
        .offset:         32
        .size:           8
        .value_kind:     global_buffer
      - .address_space:  global
        .offset:         40
        .size:           8
        .value_kind:     global_buffer
    .group_segment_fixed_size: 0
    .kernarg_segment_align: 8
    .kernarg_segment_size: 48
    .language:       OpenCL C
    .language_version:
      - 2
      - 0
    .max_flat_workgroup_size: 256
    .name:           _Z11k_rwkv_postPKfS0_S0_S0_S0_Pt
    .private_segment_fixed_size: 0
    .sgpr_count:     24
    .sgpr_spill_count: 0
    .symbol:         _Z11k_rwkv_postPKfS0_S0_S0_S0_Pt.kd
    .uniform_work_group_size: 1
    .uses_dynamic_stack: false
    .vgpr_count:     32
    .vgpr_spill_count: 0
    .wavefront_size: 64
  - .agpr_count:     0
    .args:
      - .address_space:  global
        .offset:         0
        .size:           8
        .value_kind:     global_buffer
      - .address_space:  global
        .offset:         8
        .size:           8
        .value_kind:     global_buffer
      - .address_space:  global
        .offset:         16
        .size:           8
        .value_kind:     global_buffer
      - .address_space:  global
        .offset:         24
        .size:           8
        .value_kind:     global_buffer
    .group_segment_fixed_size: 0
    .kernarg_segment_align: 8
    .kernarg_segment_size: 32
    .language:       OpenCL C
    .language_version:
      - 2
      - 0
    .max_flat_workgroup_size: 64
    .name:           _Z6k_attnPKtS0_S0_Pt
    .private_segment_fixed_size: 0
    .sgpr_count:     25
    .sgpr_spill_count: 0
    .symbol:         _Z6k_attnPKtS0_S0_Pt.kd
    .uniform_work_group_size: 1
    .uses_dynamic_stack: false
    .vgpr_count:     177
    .vgpr_spill_count: 0
    .wavefront_size: 64
  - .agpr_count:     0
    .args:
      - .address_space:  global
        .offset:         0
        .size:           8
        .value_kind:     global_buffer
      - .address_space:  global
        .offset:         8
        .size:           8
        .value_kind:     global_buffer
      - .address_space:  global
        .offset:         16
        .size:           8
        .value_kind:     global_buffer
      - .address_space:  global
        .offset:         24
        .size:           8
        .value_kind:     global_buffer
    .group_segment_fixed_size: 4
    .kernarg_segment_align: 8
    .kernarg_segment_size: 32
    .language:       OpenCL C
    .language_version:
      - 2
      - 0
    .max_flat_workgroup_size: 256
    .name:           _Z11k_diff_postPKtPKfS2_Pt
    .private_segment_fixed_size: 0
    .sgpr_count:     20
    .sgpr_spill_count: 0
    .symbol:         _Z11k_diff_postPKtPKfS2_Pt.kd
    .uniform_work_group_size: 1
    .uses_dynamic_stack: false
    .vgpr_count:     23
    .vgpr_spill_count: 0
    .wavefront_size: 64
  - .agpr_count:     0
    .args:
      - .address_space:  global
        .offset:         0
        .size:           8
        .value_kind:     global_buffer
      - .address_space:  global
        .offset:         8
        .size:           8
        .value_kind:     global_buffer
    .group_segment_fixed_size: 0
    .kernarg_segment_align: 8
    .kernarg_segment_size: 16
    .language:       OpenCL C
    .language_version:
      - 2
      - 0
    .max_flat_workgroup_size: 256
    .name:           _Z13k_softmax_memPKfPt
    .private_segment_fixed_size: 0
    .sgpr_count:     14
    .sgpr_spill_count: 0
    .symbol:         _Z13k_softmax_memPKfPt.kd
    .uniform_work_group_size: 1
    .uses_dynamic_stack: false
    .vgpr_count:     17
    .vgpr_spill_count: 0
    .wavefront_size: 64
  - .agpr_count:     0
    .args:
      - .address_space:  global
        .offset:         0
        .size:           8
        .value_kind:     global_buffer
      - .address_space:  global
        .offset:         8
        .size:           8
        .value_kind:     global_buffer
      - .address_space:  global
        .offset:         16
        .size:           8
        .value_kind:     global_buffer
      - .address_space:  global
        .offset:         24
        .size:           8
        .value_kind:     global_buffer
      - .address_space:  global
        .offset:         32
        .size:           8
        .value_kind:     global_buffer
      - .address_space:  global
        .offset:         40
        .size:           8
        .value_kind:     global_buffer
      - .address_space:  global
        .offset:         48
        .size:           8
        .value_kind:     global_buffer
      - .address_space:  global
        .offset:         56
        .size:           8
        .value_kind:     global_buffer
      - .address_space:  global
        .offset:         64
        .size:           8
        .value_kind:     global_buffer
      - .address_space:  global
        .offset:         72
        .size:           8
        .value_kind:     global_buffer
      - .address_space:  global
        .offset:         80
        .size:           8
        .value_kind:     global_buffer
    .group_segment_fixed_size: 8496
    .kernarg_segment_align: 8
    .kernarg_segment_size: 88
    .language:       OpenCL C
    .language_version:
      - 2
      - 0
    .max_flat_workgroup_size: 256
    .name:           _Z8k_routerPKfS0_S0_S0_S0_S0_PtPjPiS3_Pf
    .private_segment_fixed_size: 0
    .sgpr_count:     30
    .sgpr_spill_count: 0
    .symbol:         _Z8k_routerPKfS0_S0_S0_S0_S0_PtPjPiS3_Pf.kd
    .uniform_work_group_size: 1
    .uses_dynamic_stack: false
    .vgpr_count:     37
    .vgpr_spill_count: 0
    .wavefront_size: 64
  - .agpr_count:     0
    .args:
      - .address_space:  global
        .offset:         0
        .size:           8
        .value_kind:     global_buffer
    .group_segment_fixed_size: 0
    .kernarg_segment_align: 8
    .kernarg_segment_size: 8
    .language:       OpenCL C
    .language_version:
      - 2
      - 0
    .max_flat_workgroup_size: 1024
    .name:           _Z13k_moe_offsetsPj
    .private_segment_fixed_size: 0
    .sgpr_count:     24
    .sgpr_spill_count: 0
    .symbol:         _Z13k_moe_offsetsPj.kd
    .uniform_work_group_size: 1
    .uses_dynamic_stack: false
    .vgpr_count:     4
    .vgpr_spill_count: 0
    .wavefront_size: 64
  - .agpr_count:     0
    .args:
      - .address_space:  global
        .offset:         0
        .size:           8
        .value_kind:     global_buffer
      - .address_space:  global
        .offset:         8
        .size:           8
        .value_kind:     global_buffer
      - .address_space:  global
        .offset:         16
        .size:           8
        .value_kind:     global_buffer
      - .address_space:  global
        .offset:         24
        .size:           8
        .value_kind:     global_buffer
      - .address_space:  global
        .offset:         32
        .size:           8
        .value_kind:     global_buffer
    .group_segment_fixed_size: 0
    .kernarg_segment_align: 8
    .kernarg_segment_size: 40
    .language:       OpenCL C
    .language_version:
      - 2
      - 0
    .max_flat_workgroup_size: 256
    .name:           _Z8k_gatherPKtPKjPKiS4_Pt
    .private_segment_fixed_size: 0
    .sgpr_count:     20
    .sgpr_spill_count: 0
    .symbol:         _Z8k_gatherPKtPKjPKiS4_Pt.kd
    .uniform_work_group_size: 1
    .uses_dynamic_stack: false
    .vgpr_count:     10
    .vgpr_spill_count: 0
    .wavefront_size: 64
  - .agpr_count:     0
    .args:
      - .address_space:  global
        .offset:         0
        .size:           8
        .value_kind:     global_buffer
      - .address_space:  global
        .offset:         8
        .size:           8
        .value_kind:     global_buffer
      - .address_space:  global
        .offset:         16
        .size:           8
        .value_kind:     global_buffer
      - .offset:         24
        .size:           4
        .value_kind:     hidden_block_count_x
      - .offset:         28
        .size:           4
        .value_kind:     hidden_block_count_y
      - .offset:         32
        .size:           4
        .value_kind:     hidden_block_count_z
      - .offset:         36
        .size:           2
        .value_kind:     hidden_group_size_x
      - .offset:         38
        .size:           2
        .value_kind:     hidden_group_size_y
      - .offset:         40
        .size:           2
        .value_kind:     hidden_group_size_z
      - .offset:         42
        .size:           2
        .value_kind:     hidden_remainder_x
      - .offset:         44
        .size:           2
        .value_kind:     hidden_remainder_y
      - .offset:         46
        .size:           2
        .value_kind:     hidden_remainder_z
      - .offset:         64
        .size:           8
        .value_kind:     hidden_global_offset_x
      - .offset:         72
        .size:           8
        .value_kind:     hidden_global_offset_y
      - .offset:         80
        .size:           8
        .value_kind:     hidden_global_offset_z
      - .offset:         88
        .size:           2
        .value_kind:     hidden_grid_dims
    .group_segment_fixed_size: 0
    .kernarg_segment_align: 8
    .kernarg_segment_size: 280
    .language:       OpenCL C
    .language_version:
      - 2
      - 0
    .max_flat_workgroup_size: 1024
    .name:           _Z10k_silu_mulPKfPKjPt
    .private_segment_fixed_size: 0
    .sgpr_count:     16
    .sgpr_spill_count: 0
    .symbol:         _Z10k_silu_mulPKfPKjPt.kd
    .uniform_work_group_size: 1
    .uses_dynamic_stack: false
    .vgpr_count:     10
    .vgpr_spill_count: 0
    .wavefront_size: 64
  - .agpr_count:     0
    .args:
      - .address_space:  global
        .offset:         0
        .size:           8
        .value_kind:     global_buffer
      - .address_space:  global
        .offset:         8
        .size:           8
        .value_kind:     global_buffer
      - .address_space:  global
        .offset:         16
        .size:           8
        .value_kind:     global_buffer
      - .address_space:  global
        .offset:         24
        .size:           8
        .value_kind:     global_buffer
      - .address_space:  global
        .offset:         32
        .size:           8
        .value_kind:     global_buffer
      - .address_space:  global
        .offset:         40
        .size:           8
        .value_kind:     global_buffer
      - .address_space:  global
        .offset:         48
        .size:           8
        .value_kind:     global_buffer
      - .address_space:  global
        .offset:         56
        .size:           8
        .value_kind:     global_buffer
    .group_segment_fixed_size: 16
    .kernarg_segment_align: 8
    .kernarg_segment_size: 64
    .language:       OpenCL C
    .language_version:
      - 2
      - 0
    .max_flat_workgroup_size: 256
    .name:           _Z7k_finalPKfS0_PKjPKiS4_S0_S0_Pf
    .private_segment_fixed_size: 0
    .sgpr_count:     30
    .sgpr_spill_count: 0
    .symbol:         _Z7k_finalPKfS0_PKjPKiS4_S0_S0_Pf.kd
    .uniform_work_group_size: 1
    .uses_dynamic_stack: false
    .vgpr_count:     35
    .vgpr_spill_count: 0
    .wavefront_size: 64
  - .agpr_count:     0
    .args:
      - .address_space:  global
        .offset:         0
        .size:           8
        .value_kind:     global_buffer
      - .offset:         8
        .size:           4
        .value_kind:     by_value
      - .address_space:  global
        .offset:         16
        .size:           8
        .value_kind:     global_buffer
      - .offset:         24
        .size:           4
        .value_kind:     by_value
      - .offset:         28
        .size:           4
        .value_kind:     by_value
      - .offset:         32
        .size:           24
        .value_kind:     by_value
      - .address_space:  global
        .offset:         56
        .size:           8
        .value_kind:     global_buffer
      - .offset:         64
        .size:           4
        .value_kind:     by_value
    .group_segment_fixed_size: 17408
    .kernarg_segment_align: 8
    .kernarg_segment_size: 68
    .language:       OpenCL C
    .language_version:
      - 2
      - 0
    .max_flat_workgroup_size: 256
    .name:           _Z6k_gemmI10NEpiInProjEvPKtiS2_iiT_PKji
    .private_segment_fixed_size: 0
    .sgpr_count:     27
    .sgpr_spill_count: 0
    .symbol:         _Z6k_gemmI10NEpiInProjEvPKtiS2_iiT_PKji.kd
    .uniform_work_group_size: 1
    .uses_dynamic_stack: false
    .vgpr_count:     44
    .vgpr_spill_count: 0
    .wavefront_size: 64
  - .agpr_count:     0
    .args:
      - .address_space:  global
        .offset:         0
        .size:           8
        .value_kind:     global_buffer
      - .offset:         8
        .size:           4
        .value_kind:     by_value
      - .address_space:  global
        .offset:         16
        .size:           8
        .value_kind:     global_buffer
      - .offset:         24
        .size:           4
        .value_kind:     by_value
      - .offset:         28
        .size:           4
        .value_kind:     by_value
      - .offset:         32
        .size:           16
        .value_kind:     by_value
      - .address_space:  global
        .offset:         48
        .size:           8
        .value_kind:     global_buffer
      - .offset:         56
        .size:           4
        .value_kind:     by_value
    .group_segment_fixed_size: 17408
    .kernarg_segment_align: 8
    .kernarg_segment_size: 60
    .language:       OpenCL C
    .language_version:
      - 2
      - 0
    .max_flat_workgroup_size: 256
    .name:           _Z6k_gemmI6NEpiBfEvPKtiS2_iiT_PKji
    .private_segment_fixed_size: 0
    .sgpr_count:     21
    .sgpr_spill_count: 0
    .symbol:         _Z6k_gemmI6NEpiBfEvPKtiS2_iiT_PKji.kd
    .uniform_work_group_size: 1
    .uses_dynamic_stack: false
    .vgpr_count:     44
    .vgpr_spill_count: 0
    .wavefront_size: 64
  - .agpr_count:     0
    .args:
      - .address_space:  global
        .offset:         0
        .size:           8
        .value_kind:     global_buffer
      - .offset:         8
        .size:           4
        .value_kind:     by_value
      - .address_space:  global
        .offset:         16
        .size:           8
        .value_kind:     global_buffer
      - .offset:         24
        .size:           4
        .value_kind:     by_value
      - .offset:         28
        .size:           4
        .value_kind:     by_value
      - .offset:         32
        .size:           24
        .value_kind:     by_value
      - .address_space:  global
        .offset:         56
        .size:           8
        .value_kind:     global_buffer
      - .offset:         64
        .size:           4
        .value_kind:     by_value
    .group_segment_fixed_size: 17408
    .kernarg_segment_align: 8
    .kernarg_segment_size: 68
    .language:       OpenCL C
    .language_version:
      - 2
      - 0
    .max_flat_workgroup_size: 256
    .name:           _Z6k_gemmI9NEpiResidEvPKtiS2_iiT_PKji
    .private_segment_fixed_size: 0
    .sgpr_count:     21
    .sgpr_spill_count: 0
    .symbol:         _Z6k_gemmI9NEpiResidEvPKtiS2_iiT_PKji.kd
    .uniform_work_group_size: 1
    .uses_dynamic_stack: false
    .vgpr_count:     44
    .vgpr_spill_count: 0
    .wavefront_size: 64
  - .agpr_count:     0
    .args:
      - .address_space:  global
        .offset:         0
        .size:           8
        .value_kind:     global_buffer
      - .offset:         8
        .size:           4
        .value_kind:     by_value
      - .address_space:  global
        .offset:         16
        .size:           8
        .value_kind:     global_buffer
      - .offset:         24
        .size:           4
        .value_kind:     by_value
      - .offset:         28
        .size:           4
        .value_kind:     by_value
      - .offset:         32
        .size:           16
        .value_kind:     by_value
      - .address_space:  global
        .offset:         48
        .size:           8
        .value_kind:     global_buffer
      - .offset:         56
        .size:           4
        .value_kind:     by_value
    .group_segment_fixed_size: 17408
    .kernarg_segment_align: 8
    .kernarg_segment_size: 60
    .language:       OpenCL C
    .language_version:
      - 2
      - 0
    .max_flat_workgroup_size: 256
    .name:           _Z6k_gemmI7NEpiF32EvPKtiS2_iiT_PKji
    .private_segment_fixed_size: 0
    .sgpr_count:     21
    .sgpr_spill_count: 0
    .symbol:         _Z6k_gemmI7NEpiF32EvPKtiS2_iiT_PKji.kd
    .uniform_work_group_size: 1
    .uses_dynamic_stack: false
    .vgpr_count:     44
    .vgpr_spill_count: 0
    .wavefront_size: 64
